# attention key loop: q-fragment wait moved to the task prologue so the per-chunk staging loads are no longer waited right after issue; P4a weight-tile X loads issued one at a time across the prep stage
# speedup vs baseline: 1.0237x; 1.0104x over previous
; #define GAS __attribute__((address_space(1)))
; #define AT_STAGE_LOAD(kc_) do { kreg = *(const GAS v4u*)(PROJ + ((size_t)b * SEQ + (size_t)(kc_) * 64 + srow) * PROJ_LD + PJ_K + h * 64 + spc * 8); \
;                                 vreg = *(const GAS v4u*)(VT + (size_t)(h * 64 + srow) * T + (size_t)b * SEQ + (size_t)(kc_) * 64 + spc * 8); } while (0)
; #define AT_STAGE_WRITE(buf_) do { *(LAS v4u*)(F.lds + A_KOFF + (buf_) * AKV + srow * 144 + spc * 16) = kreg; *(LAS v4u*)(F.lds + A_VOFF + (buf_) * AKV + srow * 144 + spc * 16) = vreg; } while (0)
; __device__ __forceinline__ void p2_shift_attn(Frame& F0, const In& I) {
;     ...
;     for (int task = F.vcu; task < BATCH * AH * (SEQ / 256); task += F.G) {
;         const int bh = task >> 5, q256 = task & 31, b = bh >> 4, h = bh & 15, c0 = q256 * 4;
;         const int q0 = q256 * 256 + F.wave * 32, cw = c0 + (F.wave >> 1);
;         const int kc_lo = (c0 > LEFT) ? c0 - LEFT : 0, kc_hi = c0 + 3;
;         __syncthreads();
;         if (F.tid < REL_TABLE) tbl[F.tid] = I.rel_bias[h * REL_TABLE + F.tid];
;         const size_t tokq = (size_t)b * SEQ + q0 + r;
;         bf16x8 qf[4];
; #pragma unroll
;         for (int s = 0; s < 4; ++s) qf[s] = *(const GAS bf16x8*)(PROJ + tokq * PROJ_LD + PJ_Q + h * 64 + 16 * s + 8 * hh);
;         f32x16 o0, o1;
; #pragma unroll
;         for (int i = 0; i < 16; ++i) { o0[i] = 0.f; o1[i] = 0.f; }
;         float m_run = -1e30f, l_run = 0.f;
;         v4u kreg, vreg;
;     ...
;         AT_STAGE_LOAD(kc_lo); AT_STAGE_WRITE(0);
;         __syncthreads();
.LBB0_878:
	s_or_b64 exec, exec, s[12:13]
	v_readlane_b32 s100, v254, 9
	v_readlane_b32 s101, v254, 10
	s_mul_i32 s98, s16, 0x140
	s_add_i32 s98, s98, 319
	s_lshl_b32 s98, s98, 2
	s_nop 4
	s_load_dword s99, s[100:101], s98
	s_waitcnt lgkmcnt(0)
	v_mov_b32_e32 v177, s99
	ds_write_b32 v125, v177 offset:42240
	s_and_b32 s8, s26, 31
	s_lshl_b32 s28, s8, 2
	s_lshl_b32 s12, s8, 8
	s_ashr_i32 s14, s26, 9
	s_add_i32 s13, s12, s20
	s_add_i32 s12, s28, -8
	s_cmp_gt_u32 s8, 2
	s_cselect_b32 s12, s12, 0
	s_ashr_i32 s15, s14, 31
	s_or_b32 s27, s28, 3
	s_lshl_b64 s[18:19], s[14:15], 13
	s_ashr_i32 s8, s13, 31
	s_add_u32 s13, s18, s13
	v_or_b32_e32 v140, s13, v124
	s_addc_u32 s29, s19, s8
	v_mad_u64_u32 v[4:5], s[30:31], v140, s23, v[134:135]
	s_ashr_i32 s13, s12, 31
	s_lshl_b32 s8, s16, 6
	s_lshl_b32 s16, s16, 7
	s_lshl_b64 s[30:31], s[12:13], 6
	s_add_u32 s18, s30, s18
	s_addc_u32 s19, s31, s19
	v_lshl_add_u64 v[6:7], s[18:19], 0, v[126:127]
	v_mad_u64_u32 v[8:9], s[18:19], v6, s23, v[134:135]
	s_mov_b32 s17, s9
	v_mad_i32_i24 v9, v7, s23, v9
	v_lshl_add_u64 v[6:7], v[8:9], 0, s[16:17]
	v_add_u32_e32 v8, s8, v126
	v_ashrrev_i32_e32 v9, 31, v8
	v_mad_i32_i24 v5, s29, v167, v5
	v_lshlrev_b64 v[8:9], 16, v[8:9]
	v_lshl_add_u64 v[4:5], v[4:5], 0, s[16:17]
	v_lshl_add_u64 v[8:9], s[0:1], 0, v[8:9]
	s_lshl_b64 s[16:17], s[14:15], 14
	v_lshl_add_u64 v[8:9], v[8:9], 0, s[16:17]
	s_lshl_b64 s[18:19], s[12:13], 7
	v_lshl_add_u64 v[6:7], v[6:7], 0, v[138:139]
	v_lshl_add_u64 v[8:9], v[8:9], 0, s[18:19]
	v_lshl_add_u64 v[4:5], v[4:5], 0, v[136:137]
	v_lshl_add_u64 v[8:9], v[8:9], 0, v[138:139]
	global_load_dwordx4 v[68:71], v[6:7], off offset:2048
	global_load_dwordx4 v[80:83], v[8:9], off
	global_load_dwordx4 v[72:75], v[4:5], off
	global_load_dwordx4 v[76:79], v[4:5], off offset:32
	global_load_dwordx4 v[84:87], v[4:5], off offset:64
	global_load_dwordx4 v[88:91], v[4:5], off offset:96
	v_mov_b32_e32 v141, s29
	s_cmp_gt_i32 s12, s27
	s_waitcnt vmcnt(5)
	ds_write_b128 v162, v[68:71] offset:2048
	s_waitcnt vmcnt(4)
	ds_write_b128 v162, v[80:83] offset:20480
	s_waitcnt vmcnt(0) lgkmcnt(0)
	s_barrier
	s_cbranch_scc1 .LBB0_874
	s_lshr_b32 s13, s26, 5
	s_and_b32 s15, s25, 31
	s_lshl_b32 s15, s15, 8
	s_and_b32 s13, s13, 15
	v_lshl_add_u32 v4, s13, 6, v126
	s_lshl_b32 s30, s13, 7
	s_add_i32 s13, s28, s21
	s_add_i32 s15, s22, s15
	s_lshl_b32 s29, s12, 6
	s_add_i32 s28, s13, -8
	s_sub_i32 s29, s15, s29
	v_ashrrev_i32_e32 v5, 31, v4
	s_add_u32 s16, s18, s16
	v_lshlrev_b64 v[4:5], 16, v[4:5]
	s_addc_u32 s17, s19, s17
	v_lshl_add_u64 v[4:5], s[16:17], 0, v[4:5]
	s_mul_hi_i32 s15, s14, 0x2100000
	s_mul_i32 s14, s14, 0x2100000
	s_mul_i32 s17, s12, 0x42000
	v_mov_b32_e32 v16, v2
	v_mov_b32_e32 v17, v2
	v_lshl_add_u64 v[142:143], v[130:131], 0, v[4:5]
	s_mul_hi_i32 s16, s12, 0x42000
	s_add_u32 s14, s14, s17
	v_mov_b32_e32 v3, v2
	v_mov_b32_e32 v4, v2
	v_mov_b32_e32 v5, v2
	v_mov_b32_e32 v6, v2
	v_mov_b32_e32 v7, v2
	v_mov_b32_e32 v8, v2
	v_mov_b32_e32 v9, v2
	v_mov_b32_e32 v10, v2
	v_mov_b32_e32 v11, v2
	v_mov_b32_e32 v12, v2
	v_mov_b32_e32 v13, v2
	v_mov_b32_e32 v14, v2
	v_mov_b32_e32 v15, v2
	v_mov_b64_e32 v[34:35], v[16:17]
	s_addc_u32 s15, s15, s16
	s_or_b32 s14, s14, s30
	v_mov_b64_e32 v[32:33], v[14:15]
	v_mov_b64_e32 v[30:31], v[12:13]
	v_mov_b64_e32 v[28:29], v[10:11]
	v_mov_b64_e32 v[26:27], v[8:9]
	v_mov_b64_e32 v[24:25], v[6:7]
	v_mov_b64_e32 v[22:23], v[4:5]
	v_mov_b64_e32 v[20:21], v[2:3]
	v_mov_b64_e32 v[18:19], v[16:17]
	v_lshl_add_u64 v[144:145], v[132:133], 0, s[14:15]
	v_mov_b32_e32 v168, 0
	v_mov_b32_e32 v169, 0xf149f2ca
	v_mov_b64_e32 v[16:17], v[14:15]
	v_mov_b64_e32 v[14:15], v[12:13]
	v_mov_b64_e32 v[12:13], v[10:11]
	v_mov_b64_e32 v[10:11], v[8:9]
	v_mov_b64_e32 v[8:9], v[6:7]
	v_mov_b64_e32 v[6:7], v[4:5]
	v_mov_b64_e32 v[4:5], v[2:3]

; #define LAS __attribute__((address_space(3)))
; __device__ __forceinline__ void p2_shift_attn(Frame& F0, const In& I) {
;     ...
;         for (int kc = kc_lo; kc <= kc_hi; ++kc) {
;             const int buf = (kc - kc_lo) & 1;
;             if (kc < kc_hi) AT_STAGE_LOAD(kc + 1);
;             if (kc >= cw - LEFT && kc <= cw) {
;                 const LAS unsigned char* Kb = F.lds + A_KOFF + buf * AKV; const LAS unsigned char* Vb = F.lds + A_VOFF + buf * AKV;
;                 bf16x8 kf[2][4];
; #pragma unroll
;                 for (int tt = 0; tt < 2; ++tt)
; #pragma unroll
;                     for (int s = 0; s < 4; ++s) kf[tt][s] = *(const LAS bf16x8*)(Kb + (32 * tt + rp) * 144 + 32 * s + 16 * hh);
;                 f32x16 st[2];
; #pragma unroll
;                 for (int tt = 0; tt < 2; ++tt)
; #pragma unroll
;                     for (int i = 0; i < 16; ++i) st[tt][i] = 0.f;
; #pragma unroll
;                 for (int s = 0; s < 4; ++s) { st[0] = __builtin_amdgcn_mfma_f32_32x32x16_bf16(kf[0][s], qf[s], st[0], 0, 0, 0); st[1] = __builtin_amdgcn_mfma_f32_32x32x16_bf16(kf[1][s], qf[s], st[1], 0, 0, 0); }
;                 bf16x8 va[2][2], vb[2][2];
; #pragma unroll
;                 for (int tt = 0; tt < 2; ++tt)
; #pragma unroll
;                     for (int s2 = 0; s2 < 2; ++s2) { va[tt][s2] = *(const LAS bf16x8*)(Vb + r * 144 + 64 * tt + 32 * s2 + 16 * hh); vb[tt][s2] = *(const LAS bf16x8*)(Vb + (32 + r) * 144 + 64 * tt + 32 * s2 + 16 * hh); }
;                 float mx = -1e30f;
; #pragma unroll
;                 for (int tt = 0; tt < 2; ++tt) {
;                     const int kpos0 = kc * 64 + 32 * tt;
;                     const int dbase = (q0 + r) - (kpos0 + 8 * hh);
;                     if (q0 - (kpos0 + 31) >= MAX_PAST) {
;                         const float bc = tbl[MAX_PAST + 63];
; #pragma unroll
;                         for (int i = 0; i < 16; ++i) { st[tt][i] += bc; mx = fmaxf(mx, st[tt][i]); }
;                     } else {
; #pragma unroll
;                         for (int i = 0; i < 16; ++i) { int d = dbase - (16 * (i >> 3) + 4 * ((i >> 2) & 1) + (i & 3)); d = d < MAX_PAST ? d : MAX_PAST; st[tt][i] += tbl[d + 63]; mx = fmaxf(mx, st[tt][i]); }
.LBB0_882:
	s_and_b32 s30, s12, 1
	s_cmp_lt_i32 s12, s28
	s_cselect_b64 s[18:19], -1, 0
	s_cmp_gt_i32 s12, s13
	s_cselect_b64 s[34:35], -1, 0
	s_or_b64 s[18:19], s[18:19], s[34:35]
	s_and_b64 vcc, exec, s[18:19]
	s_cbranch_vccnz .LBB0_885
	s_mul_i32 s18, s30, 0x2400
	v_add_u32_e32 v3, s18, v164
	ds_read_b128 v[36:39], v3 offset:6656
	ds_read_b128 v[52:55], v3 offset:6688
	s_add_i32 s31, s29, 32
	s_cmpk_gt_i32 s31, 0xff
	s_waitcnt lgkmcnt(1)
	v_mfma_f32_32x32x16_bf16 v[36:51], v[36:39], v[72:75], 0
	s_waitcnt lgkmcnt(0)
	v_mfma_f32_32x32x16_bf16 v[36:51], v[52:55], v[76:79], v[36:51]
	ds_read_b128 v[52:55], v3 offset:6720
	ds_read_b128 v[56:59], v3 offset:6752
	s_waitcnt lgkmcnt(1)
	v_mfma_f32_32x32x16_bf16 v[36:51], v[52:55], v[84:87], v[36:51]
	ds_read_b128 v[52:55], v3 offset:2048
	ds_read_b128 v[92:95], v3 offset:2080
	s_waitcnt lgkmcnt(2)
	v_mfma_f32_32x32x16_bf16 v[36:51], v[56:59], v[88:91], v[36:51]
	s_waitcnt lgkmcnt(1)
	v_mfma_f32_32x32x16_bf16 v[52:67], v[52:55], v[72:75], 0
	s_waitcnt lgkmcnt(0)
	v_mfma_f32_32x32x16_bf16 v[52:67], v[92:95], v[76:79], v[52:67]
	ds_read_b128 v[92:95], v3 offset:2112
	ds_read_b128 v[172:175], v3 offset:2144
	v_add_u32_e32 v3, s18, v165
	ds_read_b128 v[120:123], v3 offset:20480
	ds_read_b128 v[112:115], v3 offset:20512
	ds_read_b128 v[116:119], v3 offset:25088
	ds_read_b128 v[108:111], v3 offset:25120
	s_mov_b64 s[18:19], -1
	s_waitcnt lgkmcnt(5)
	v_mfma_f32_32x32x16_bf16 v[52:67], v[92:95], v[84:87], v[52:67]
	ds_read_b128 v[104:107], v3 offset:20544
	ds_read_b128 v[96:99], v3 offset:20576
	ds_read_b128 v[100:103], v3 offset:25152
	ds_read_b128 v[92:95], v3 offset:25184
	v_add_u32_e32 v3, s29, v166
	v_add_u32_e32 v178, 0x80, v3
	v_lshlrev_b32_e32 v178, 2, v178
	s_waitcnt lgkmcnt(8)
	v_mfma_f32_32x32x16_bf16 v[52:67], v[172:175], v[88:91], v[52:67]
	s_cbranch_scc1 .LBB0_889
	ds_read_b32 v146, v178 offset:40952
	ds_read_b32 v147, v178 offset:40948
	ds_read_b32 v148, v178 offset:40944
	ds_read_b32 v149, v178 offset:40940
	ds_read_b32 v154, v178 offset:40936
	ds_read_b32 v155, v178 offset:40932
	ds_read_b32 v156, v178 offset:40928
	ds_read_b32 v157, v178 offset:40924
	s_waitcnt lgkmcnt(6)
	v_pk_add_f32 v[152:153], v[52:53], v[146:147]
	s_waitcnt lgkmcnt(4)
	v_pk_add_f32 v[150:151], v[54:55], v[148:149]
	v_max3_f32 v146, v152, s24, v153
	v_max3_f32 v148, v146, v150, v151
	s_waitcnt lgkmcnt(2)
	v_pk_add_f32 v[146:147], v[56:57], v[154:155]
	v_max3_f32 v154, v148, v146, v147
	s_waitcnt lgkmcnt(0)
	v_pk_add_f32 v[148:149], v[58:59], v[156:157]
	v_max3_f32 v160, v154, v148, v149
	ds_read_b32 v154, v178 offset:40888
	ds_read_b32 v155, v178 offset:40884
	ds_read_b32 v156, v178 offset:40880
	ds_read_b32 v157, v178 offset:40876
	ds_read_b32 v170, v178 offset:40872
	ds_read_b32 v171, v178 offset:40868
	ds_read_b32 v172, v178 offset:40864
	ds_read_b32 v173, v178 offset:40860
	s_waitcnt lgkmcnt(6)
	v_pk_add_f32 v[158:159], v[60:61], v[154:155]
	s_nop 0
	v_max3_f32 v154, v160, v158, v159
	s_waitcnt lgkmcnt(4)
	v_pk_add_f32 v[160:161], v[62:63], v[156:157]
	s_nop 0
	v_max3_f32 v156, v154, v160, v161
	s_waitcnt lgkmcnt(2)
	v_pk_add_f32 v[154:155], v[64:65], v[170:171]
	s_nop 0
	v_max3_f32 v170, v156, v154, v155
	s_waitcnt lgkmcnt(0)
	v_pk_add_f32 v[156:157], v[66:67], v[172:173]
	s_nop 0
	v_max3_f32 v170, v170, v156, v157
	s_cbranch_execnz .LBB0_891
	s_branch .LBB0_890

; __device__ __forceinline__ void p4a_chunk(Frame& F0, const In& I) {
;     ...
;     for (int unit = F.vcu; unit < BATCH * RH * (SEQ / 64); unit += F.G, ++uit) {
;         const int bh = unit >> 7, ck = unit & 127, b = bh >> 4, h = bh & 15;
;         const size_t tok0 = (size_t)b * SEQ + (size_t)ck * 64 + 8 * w;
;         const int hc = h * 64 + lane;
;         float lwv[8], ic[8], rr[8], kk[8], vv[8];
; #pragma unroll
;         for (int i = 0; i < 8; ++i) { const size_t tok = tok0 + i; lwv[i] = LW[tok * RW + hc]; ic[i] = bf2f(ICL[tok * RW + hc]);
;             rr[i] = bf2f(RKV[tok * (3 * RW) + hc]); kk[i] = bf2f(RKV[tok * (3 * RW) + RW + hc]); vv[i] = bf2f(RKV[tok * (3 * RW) + 2 * RW + hc]); }
;         const float kkp = I.k_k[hc], kap = I.k_a[hc];
.LBB0_1083:
	s_ashr_i32 s14, s13, 11
	s_ashr_i32 s15, s14, 31
	s_lshl_b64 s[14:15], s[14:15], 13
	s_and_b32 s16, s33, 0x1fc0
	s_add_u32 s16, s16, s22
	s_addc_u32 s17, 0, s23
	s_add_u32 s14, s16, s14
	s_addc_u32 s15, s17, s15
	s_lshr_b32 s16, s13, 1
	s_and_b32 s16, s16, 0x3c0
	s_waitcnt vmcnt(12)
	v_readlane_b32 s56, v254, 27
	v_readlane_b32 s57, v254, 28
	v_or_b32_e32 v88, s16, v1
	s_lshl_b64 s[16:17], s[14:15], 10
	v_or_b32_e32 v82, s16, v88
	s_mulk_i32 s15, 0x1800
	s_mul_hi_u32 s16, s14, 0x1800
	v_mov_b32_e32 v83, s17
	s_add_i32 s16, s16, s15
	s_mulk_i32 s14, 0x1800
	v_readlane_b32 s20, v254, 54
	v_lshl_add_u64 v[80:81], v[82:83], 2, s[0:1]
	v_readlane_b32 s21, v254, 55
	s_add_u32 s14, s20, s14
	global_load_dword v89, v[80:81], off
	v_lshl_add_u64 v[80:81], v[82:83], 1, s[88:89]
	s_addc_u32 s15, s21, s16
	v_lshlrev_b32_e32 v68, 1, v88
	global_load_ushort v84, v[80:81], off
	v_lshl_add_u64 v[80:81], s[14:15], 0, v[68:69]
	global_load_ushort v90, v68, s[14:15]
	global_load_ushort v85, v68, s[14:15] offset:2048
	s_movk_i32 s14, 0x1000
	v_add_co_u32_e32 v86, vcc, s14, v80
	s_mov_b64 s[14:15], 0x400
	v_lshl_add_u64 v[92:93], v[82:83], 0, s[14:15]
	v_addc_co_u32_e32 v87, vcc, 0, v81, vcc
	v_lshl_add_u64 v[94:95], v[92:93], 2, s[0:1]
	v_lshl_add_u64 v[92:93], v[92:93], 1, s[88:89]
	s_movk_i32 s14, 0x2000
	global_load_ushort v168, v[86:87], off
	v_readlane_b32 s48, v254, 21
	global_load_dword v94, v[94:95], off
	v_lshlrev_b32_e32 v68, 2, v88
	global_load_ushort v95, v[92:93], off
	v_lshl_add_u64 v[92:93], v[80:81], 0, s[78:79]
	global_load_ushort v96, v[86:87], off offset:2048
	global_load_ushort v91, v[92:93], off offset:2048
	v_add_co_u32_e32 v86, vcc, s14, v80
	s_mov_b64 s[14:15], 0x800
	s_nop 0
	v_addc_co_u32_e32 v87, vcc, 0, v81, vcc
	global_load_ushort v169, v[86:87], off offset:2048
	v_lshl_add_u64 v[86:87], v[82:83], 0, s[14:15]
	v_lshl_add_u64 v[92:93], v[86:87], 2, s[0:1]
	v_lshl_add_u64 v[86:87], v[86:87], 1, s[88:89]
	s_mov_b64 s[14:15], 0x3000
	global_load_dword v104, v[92:93], off
	global_load_ushort v97, v[86:87], off
	v_lshl_add_u64 v[86:87], v[80:81], 0, s[14:15]
	s_movk_i32 s14, 0x4000
	v_add_co_u32_e32 v92, vcc, s14, v80
	s_mov_b64 s[14:15], 0xc00
	s_nop 0
	v_addc_co_u32_e32 v93, vcc, 0, v81, vcc
	global_load_ushort v99, v[92:93], off offset:-4096
	global_load_ushort v98, v[86:87], off offset:2048
	global_load_ushort v170, v[92:93], off
	v_lshl_add_u64 v[86:87], v[82:83], 0, s[14:15]
	v_lshl_add_u64 v[100:101], v[86:87], 2, s[0:1]
	v_lshl_add_u64 v[86:87], v[86:87], 1, s[88:89]
	s_mov_b64 s[14:15], 0x4800
	global_load_dword v105, v[100:101], off
	global_load_ushort v102, v[86:87], off
	v_lshl_add_u64 v[86:87], v[80:81], 0, s[14:15]
	s_movk_i32 s14, 0x5000
	global_load_ushort v106, v[92:93], off offset:2048
	global_load_ushort v103, v[86:87], off offset:2048
	v_add_co_u32_e32 v86, vcc, s14, v80
	s_mov_b64 s[14:15], 0x1000
	s_nop 0
	v_addc_co_u32_e32 v87, vcc, 0, v81, vcc
	global_load_ushort v171, v[86:87], off offset:2048
	v_lshl_add_u64 v[86:87], v[82:83], 0, s[14:15]
	v_lshl_add_u64 v[92:93], v[86:87], 2, s[0:1]
	v_lshl_add_u64 v[86:87], v[86:87], 1, s[88:89]
	s_mov_b64 s[14:15], 0x6000
	global_load_dword v108, v[92:93], off
	global_load_ushort v110, v[86:87], off
	v_lshl_add_u64 v[86:87], v[80:81], 0, s[14:15]
	s_movk_i32 s14, 0x7000
	v_add_co_u32_e32 v92, vcc, s14, v80
	s_mov_b64 s[14:15], 0x1400
	s_nop 0
	v_addc_co_u32_e32 v93, vcc, 0, v81, vcc
	global_load_ushort v112, v[92:93], off offset:-4096
	global_load_ushort v107, v[86:87], off offset:2048
	global_load_ushort v172, v[92:93], off
	v_lshl_add_u64 v[86:87], v[82:83], 0, s[14:15]
	v_lshl_add_u64 v[100:101], v[86:87], 2, s[0:1]
	v_lshl_add_u64 v[86:87], v[86:87], 1, s[88:89]
	s_mov_b64 s[14:15], 0x7800
	global_load_dword v100, v[100:101], off
	v_readlane_b32 s50, v254, 23
	global_load_ushort v113, v[86:87], off
	v_lshl_add_u64 v[86:87], v[80:81], 0, s[14:15]
	s_mov_b32 s14, 0x8000
	global_load_ushort v114, v[92:93], off offset:2048
	global_load_ushort v111, v[86:87], off offset:2048
	v_add_co_u32_e32 v86, vcc, s14, v80
	s_mov_b64 s[14:15], 0x9000
	s_nop 0
	v_addc_co_u32_e32 v87, vcc, 0, v81, vcc
	global_load_ushort v173, v[86:87], off offset:2048
	v_lshl_add_u64 v[86:87], v[82:83], 0, s[78:79]
	v_lshl_add_u64 v[92:93], v[86:87], 2, s[0:1]
	v_lshl_add_u64 v[86:87], v[86:87], 1, s[88:89]
	global_load_dword v101, v[92:93], off
	global_load_ushort v176, v[86:87], off
	v_lshl_add_u64 v[86:87], v[80:81], 0, s[14:15]
	s_mov_b32 s14, 0xa000
	v_add_co_u32_e32 v92, vcc, s14, v80
	s_mov_b64 s[14:15], 0x1c00
	s_nop 0
	v_addc_co_u32_e32 v93, vcc, 0, v81, vcc
	v_lshl_add_u64 v[82:83], v[82:83], 0, s[14:15]
	global_load_ushort v177, v[92:93], off offset:-4096
	global_load_ushort v115, v[86:87], off offset:2048
	global_load_ushort v174, v[92:93], off
	v_lshl_add_u64 v[86:87], v[82:83], 2, s[0:1]
	global_load_dword v86, v[86:87], off
	v_lshl_add_u64 v[82:83], v[82:83], 1, s[88:89]
	s_mov_b64 s[14:15], 0xa800
	global_load_ushort v186, v[82:83], off
	v_lshl_add_u64 v[82:83], v[80:81], 0, s[14:15]
	s_mov_b32 s14, 0xb000
	v_add_co_u32_e32 v80, vcc, s14, v80
	v_readlane_b32 s51, v254, 24
	s_nop 0
	v_addc_co_u32_e32 v81, vcc, 0, v81, vcc
	global_load_ushort v188, v[92:93], off offset:2048
	global_load_ushort v182, v[82:83], off offset:2048
	global_load_ushort v175, v[80:81], off offset:2048
	v_readlane_b32 s52, v254, 25
	v_readlane_b32 s53, v254, 26
	global_load_dword v88, v68, s[50:51]
	s_nop 3
	global_load_dword v230, v68, s[56:57]
	global_load_dword v68, v68, s[52:53]
	s_waitcnt vmcnt(0)
; __device__ __forceinline__ float quadsum(float x) { x += dpp_f(x, 0); x += dpp_f(x, 1); return x; }
; __device__ __forceinline__ void p5_post(Frame& F0, const In& I) {
;     ...
;         float s = 0.f, bs = 0.f;
; #pragma unroll
;         for (int e = 0; e < 16; ++e) { s += y[e]; const float kp = kk[e] * (1.0f + (ic[e] - 1.0f) * p_ka[e]); bs += rr[e] * kp * p_rk[e]; }
;         s = quadsum(s); bs = quadsum(bs);
	v_lshlrev_b32_e32 v231, 16, v84
	v_lshlrev_b32_e32 v232, 16, v85
	v_lshlrev_b32_e32 v233, 16, v90
	v_add_f32_e32 v231, -1.0, v231
	v_fma_f32 v231, v231, v68, 1.0
	v_mul_f32_e32 v232, v232, v231
	v_mul_f32_e32 v233, v233, v232
	v_mul_f32_e32 v234, v233, v230
	v_lshlrev_b32_e32 v231, 16, v95
	v_lshlrev_b32_e32 v232, 16, v91
	v_lshlrev_b32_e32 v233, 16, v96
	v_add_f32_e32 v231, -1.0, v231
	v_fma_f32 v231, v231, v68, 1.0
	v_mul_f32_e32 v232, v232, v231
	v_mul_f32_e32 v233, v233, v232
	v_mul_f32_e32 v235, v233, v230
	v_lshlrev_b32_e32 v231, 16, v97
	v_lshlrev_b32_e32 v232, 16, v98
	v_lshlrev_b32_e32 v233, 16, v99
	v_add_f32_e32 v231, -1.0, v231
	v_fma_f32 v231, v231, v68, 1.0
	v_mul_f32_e32 v232, v232, v231
	v_mul_f32_e32 v233, v233, v232
	v_mul_f32_e32 v236, v233, v230
	v_lshlrev_b32_e32 v231, 16, v102
	v_lshlrev_b32_e32 v232, 16, v103
	v_lshlrev_b32_e32 v233, 16, v106
	v_add_f32_e32 v231, -1.0, v231
	v_fma_f32 v231, v231, v68, 1.0
	v_mul_f32_e32 v232, v232, v231
	v_mul_f32_e32 v233, v233, v232
	v_mul_f32_e32 v237, v233, v230
	v_lshlrev_b32_e32 v231, 16, v110
	v_lshlrev_b32_e32 v232, 16, v107
	v_lshlrev_b32_e32 v233, 16, v112
	v_add_f32_e32 v231, -1.0, v231
	v_fma_f32 v231, v231, v68, 1.0
	v_mul_f32_e32 v232, v232, v231
	v_mul_f32_e32 v233, v233, v232
	v_mul_f32_e32 v238, v233, v230
	v_lshlrev_b32_e32 v231, 16, v113
	v_lshlrev_b32_e32 v232, 16, v111
	v_lshlrev_b32_e32 v233, 16, v114
	v_add_f32_e32 v231, -1.0, v231
	v_fma_f32 v231, v231, v68, 1.0
	v_mul_f32_e32 v232, v232, v231
	v_mul_f32_e32 v233, v233, v232
	v_mul_f32_e32 v239, v233, v230
	v_lshlrev_b32_e32 v231, 16, v176
	v_lshlrev_b32_e32 v232, 16, v115
	v_lshlrev_b32_e32 v233, 16, v177
	v_add_f32_e32 v231, -1.0, v231
	v_fma_f32 v231, v231, v68, 1.0
	v_mul_f32_e32 v232, v232, v231
	v_mul_f32_e32 v233, v233, v232
	v_mul_f32_e32 v240, v233, v230
	v_lshlrev_b32_e32 v231, 16, v186
	v_lshlrev_b32_e32 v232, 16, v182
	v_lshlrev_b32_e32 v233, 16, v188
	v_add_f32_e32 v231, -1.0, v231
	v_fma_f32 v231, v231, v68, 1.0
	v_mul_f32_e32 v232, v232, v231
	v_mul_f32_e32 v233, v233, v232
	v_mul_f32_e32 v241, v233, v230
	v_add_f32_dpp v234, v234, v234 quad_perm:[1,0,3,2] row_mask:0xf bank_mask:0xf bound_ctrl:1
	v_add_f32_dpp v235, v235, v235 quad_perm:[1,0,3,2] row_mask:0xf bank_mask:0xf bound_ctrl:1
	v_add_f32_dpp v236, v236, v236 quad_perm:[1,0,3,2] row_mask:0xf bank_mask:0xf bound_ctrl:1
	v_add_f32_dpp v237, v237, v237 quad_perm:[1,0,3,2] row_mask:0xf bank_mask:0xf bound_ctrl:1
	v_add_f32_dpp v238, v238, v238 quad_perm:[1,0,3,2] row_mask:0xf bank_mask:0xf bound_ctrl:1
	v_add_f32_dpp v239, v239, v239 quad_perm:[1,0,3,2] row_mask:0xf bank_mask:0xf bound_ctrl:1
	v_add_f32_dpp v240, v240, v240 quad_perm:[1,0,3,2] row_mask:0xf bank_mask:0xf bound_ctrl:1
	v_add_f32_dpp v241, v241, v241 quad_perm:[1,0,3,2] row_mask:0xf bank_mask:0xf bound_ctrl:1
	v_add_f32_dpp v234, v234, v234 quad_perm:[2,3,0,1] row_mask:0xf bank_mask:0xf bound_ctrl:1
	v_add_f32_dpp v235, v235, v235 quad_perm:[2,3,0,1] row_mask:0xf bank_mask:0xf bound_ctrl:1
	v_add_f32_dpp v236, v236, v236 quad_perm:[2,3,0,1] row_mask:0xf bank_mask:0xf bound_ctrl:1
	v_add_f32_dpp v237, v237, v237 quad_perm:[2,3,0,1] row_mask:0xf bank_mask:0xf bound_ctrl:1
	v_add_f32_dpp v238, v238, v238 quad_perm:[2,3,0,1] row_mask:0xf bank_mask:0xf bound_ctrl:1
	v_add_f32_dpp v239, v239, v239 quad_perm:[2,3,0,1] row_mask:0xf bank_mask:0xf bound_ctrl:1
	v_add_f32_dpp v240, v240, v240 quad_perm:[2,3,0,1] row_mask:0xf bank_mask:0xf bound_ctrl:1
	v_add_f32_dpp v241, v241, v241 quad_perm:[2,3,0,1] row_mask:0xf bank_mask:0xf bound_ctrl:1
	v_add_f32_dpp v234, v234, v234 row_ror:4 row_mask:0xf bank_mask:0xf bound_ctrl:1
	v_add_f32_dpp v235, v235, v235 row_ror:4 row_mask:0xf bank_mask:0xf bound_ctrl:1
	v_add_f32_dpp v236, v236, v236 row_ror:4 row_mask:0xf bank_mask:0xf bound_ctrl:1
	v_add_f32_dpp v237, v237, v237 row_ror:4 row_mask:0xf bank_mask:0xf bound_ctrl:1
	v_add_f32_dpp v238, v238, v238 row_ror:4 row_mask:0xf bank_mask:0xf bound_ctrl:1
	v_add_f32_dpp v239, v239, v239 row_ror:4 row_mask:0xf bank_mask:0xf bound_ctrl:1
	v_add_f32_dpp v240, v240, v240 row_ror:4 row_mask:0xf bank_mask:0xf bound_ctrl:1
	v_add_f32_dpp v241, v241, v241 row_ror:4 row_mask:0xf bank_mask:0xf bound_ctrl:1
	v_add_f32_dpp v234, v234, v234 row_ror:8 row_mask:0xf bank_mask:0xf bound_ctrl:1
	v_add_f32_dpp v235, v235, v235 row_ror:8 row_mask:0xf bank_mask:0xf bound_ctrl:1
	v_add_f32_dpp v236, v236, v236 row_ror:8 row_mask:0xf bank_mask:0xf bound_ctrl:1
	v_add_f32_dpp v237, v237, v237 row_ror:8 row_mask:0xf bank_mask:0xf bound_ctrl:1
	v_add_f32_dpp v238, v238, v238 row_ror:8 row_mask:0xf bank_mask:0xf bound_ctrl:1
	v_add_f32_dpp v239, v239, v239 row_ror:8 row_mask:0xf bank_mask:0xf bound_ctrl:1
	v_add_f32_dpp v240, v240, v240 row_ror:8 row_mask:0xf bank_mask:0xf bound_ctrl:1
	v_add_f32_dpp v241, v241, v241 row_ror:8 row_mask:0xf bank_mask:0xf bound_ctrl:1
	v_readlane_b32 s58, v234, 16
	v_readlane_b32 s59, v234, 32
	v_readlane_b32 s60, v234, 48
	s_nop 1
	v_add_f32_e32 v234, s58, v234
	v_add_f32_e32 v234, s59, v234
	v_add_f32_e32 v234, s60, v234
	v_readlane_b32 s58, v235, 16
	v_readlane_b32 s59, v235, 32
	v_readlane_b32 s60, v235, 48
	s_nop 1
	v_add_f32_e32 v235, s58, v235
	v_add_f32_e32 v235, s59, v235
	v_add_f32_e32 v235, s60, v235
	v_readlane_b32 s58, v236, 16
	v_readlane_b32 s59, v236, 32
	v_readlane_b32 s60, v236, 48
	s_nop 1
	v_add_f32_e32 v236, s58, v236
	v_add_f32_e32 v236, s59, v236
	v_add_f32_e32 v236, s60, v236
	v_readlane_b32 s58, v237, 16
	v_readlane_b32 s59, v237, 32
	v_readlane_b32 s60, v237, 48
	s_nop 1
	v_add_f32_e32 v237, s58, v237
	v_add_f32_e32 v237, s59, v237
	v_add_f32_e32 v237, s60, v237
; #define LAS __attribute__((address_space(3)))
; #define CBAR() do { asm volatile("s_waitcnt lgkmcnt(0)" ::: "memory"); __builtin_amdgcn_s_barrier(); asm volatile("" ::: "memory"); } while (0)
; __device__ __forceinline__ void tr8_load(const MoeItem& m, f32x4 (&v)[16], int lane) {
;     const int kr = lane >> 4, cq = lane & 15;
;     const int voff = (kr * m.ldw + 4 * cq) * 4;
; #pragma unroll
;     for (int i = 0; i < 16; ++i) v[i] = __builtin_bit_cast(f32x4, __builtin_amdgcn_raw_buffer_load_b128(m.rs, voff, (int)(m.soff + (unsigned)i * m.rstep), 0));
; }
; __device__ __forceinline__ void p4a_chunk(Frame& F0, const In& I) {
;     ...
;         float cs[8]; { float run = 0.f;
; #pragma unroll
;             for (int i = 0; i < 8; ++i) { run += lwv[i]; cs[i] = run; } }
;         __syncthreads();
;         ((LAS float*)(L + C_SEG))[w * 64 + lane] = cs[7];
;         CBAR();
;         float pre = 0.f, tot = 0.f;
; #pragma unroll
;         for (int j = 0; j < 8; ++j) { const float sg = ((const LAS float*)(L + C_SEG))[j * 64 + lane]; tot += sg; pre += (j < w) ? sg : 0.f; }
;         if (w == 0) ((LAS float*)(L + C_GAM))[lane] = __expf(tot);
	v_readlane_b32 s58, v238, 16
	v_readlane_b32 s59, v238, 32
	v_readlane_b32 s60, v238, 48
	s_nop 1
	v_add_f32_e32 v238, s58, v238
	v_add_f32_e32 v238, s59, v238
	v_add_f32_e32 v238, s60, v238
	v_readlane_b32 s58, v239, 16
	v_readlane_b32 s59, v239, 32
	v_readlane_b32 s60, v239, 48
	s_nop 1
	v_add_f32_e32 v239, s58, v239
	v_add_f32_e32 v239, s59, v239
	v_add_f32_e32 v239, s60, v239
	v_readlane_b32 s58, v240, 16
	v_readlane_b32 s59, v240, 32
	v_readlane_b32 s60, v240, 48
	s_nop 1
	v_add_f32_e32 v240, s58, v240
	v_add_f32_e32 v240, s59, v240
	v_add_f32_e32 v240, s60, v240
	v_readlane_b32 s58, v241, 16
	v_readlane_b32 s59, v241, 32
	v_readlane_b32 s60, v241, 48
	s_nop 1
	v_add_f32_e32 v241, s58, v241
	v_add_f32_e32 v241, s59, v241
	v_add_f32_e32 v241, s60, v241
	v_mov_b32_e32 v242, 0
	v_cmp_eq_u32_e32 vcc, 0, v1
	s_nop 1
	v_cndmask_b32_e32 v242, v242, v234, vcc
	v_cmp_eq_u32_e32 vcc, 1, v1
	s_nop 1
	v_cndmask_b32_e32 v242, v242, v235, vcc
	v_cmp_eq_u32_e32 vcc, 2, v1
	s_nop 1
	v_cndmask_b32_e32 v242, v242, v236, vcc
	v_cmp_eq_u32_e32 vcc, 3, v1
	s_nop 1
	v_cndmask_b32_e32 v242, v242, v237, vcc
	v_cmp_eq_u32_e32 vcc, 4, v1
	s_nop 1
	v_cndmask_b32_e32 v242, v242, v238, vcc
	v_cmp_eq_u32_e32 vcc, 5, v1
	s_nop 1
	v_cndmask_b32_e32 v242, v242, v239, vcc
	v_cmp_eq_u32_e32 vcc, 6, v1
	s_nop 1
	v_cndmask_b32_e32 v242, v242, v240, vcc
	v_cmp_eq_u32_e32 vcc, 7, v1
	s_nop 1
	v_cndmask_b32_e32 v242, v242, v241, vcc
	s_ashr_i32 s48, s13, 11
	s_lshl_b32 s48, s48, 13
	s_lshl_b32 s49, s13, 6
	s_and_b32 s49, s49, 0x1fc0
	s_add_i32 s49, s49, s22
	s_add_i32 s48, s48, s49
	s_lshl_b32 s48, s48, 6
	s_lshr_b32 s49, s13, 5
	s_and_b32 s49, s49, 0x3c
	s_add_i32 s48, s48, s49
	v_lshl_add_u32 v243, v1, 6, s48
	s_add_u32 s50, s96, 0x1c00000
	s_addc_u32 s51, s97, 0
	s_mov_b64 s[62:63], exec
	s_mov_b64 exec, 0xff
	global_store_dword v243, v242, s[50:51]
	s_mov_b64 exec, s[62:63]
	s_cmp_gt_i32 s85, 0xffff
	s_cbranch_scc1 .Lxs_down
	s_lshr_b32 s49, s85, 11
	s_lshl_b32 s49, s49, 25
	s_bfe_u32 s54, s85, 0x50006
	s_lshl_b32 s54, s54, 20
	s_add_i32 s49, s49, s54
	s_and_b32 s54, s85, 63
	s_lshl_b32 s54, s54, 8
	s_add_i32 s49, s49, s54
	s_mov_b32 s55, 0x10000
	s_movk_i32 s56, 0x4000
	v_readlane_b32 s60, v255, 54
	v_readlane_b32 s61, v255, 55
	s_branch .Lxs_go
.Lxs_down:
	s_add_i32 s48, s85, 0xffff0000
	s_lshr_b32 s49, s48, 10
	s_lshl_b32 s49, s49, 24
	s_bfe_u32 s54, s48, 0x50005
	s_lshl_b32 s54, s54, 19
	s_add_i32 s49, s49, s54
	s_and_b32 s54, s48, 31
	s_lshl_b32 s54, s54, 8
	s_add_i32 s49, s49, s54
	s_mov_b32 s55, 0x8000
	s_movk_i32 s56, 0x2000
	v_readlane_b32 s60, v255, 52
	v_readlane_b32 s61, v255, 53
.Lxs_go:
	s_add_u32 s60, s60, s49
	s_addc_u32 s61, s61, 0
	v_mul_u32_u24_e32 v244, s56, v116
	v_lshl_or_b32 v244, v128, 2, v244
	v_mov_b32_e32 v245, 0
	v_mov_b32_e32 v246, s55
	v_mov_b32_e32 v247, 0
	v_lshl_add_u64 v[244:245], v[244:245], 0, s[60:61]
	global_load_dwordx4 v[2:5], v[244:245], off
	v_add_f32_e32 v187, 0, v89
	v_add_f32_e32 v185, v187, v94
	v_add_f32_e32 v184, v185, v104
	s_barrier
	s_andn2_b64 vcc, exec, s[24:25]
	v_readlane_b32 s49, v254, 22
	v_add_f32_e32 v183, v184, v105
	v_readlane_b32 s54, v254, 27
	v_readlane_b32 s55, v254, 28
	v_readlane_b32 s56, v254, 29
	v_readlane_b32 s57, v254, 30
	v_readlane_b32 s58, v254, 31
	v_readlane_b32 s59, v254, 32
	v_readlane_b32 s60, v254, 33
	v_readlane_b32 s61, v254, 34
	v_readlane_b32 s62, v254, 35
	v_readlane_b32 s63, v254, 36
	v_add_f32_e32 v181, v183, v108
	v_add_f32_e32 v180, v181, v100
	v_add_f32_e32 v179, v180, v101
	v_add_f32_e32 v178, v179, v86
	ds_write_b32 v117, v178
	s_waitcnt lgkmcnt(0)
	s_barrier
	ds_read2st64_b32 v[82:83], v118 offset1:1
	ds_read2st64_b32 v[86:87], v118 offset0:2 offset1:3
	ds_read2st64_b32 v[92:93], v118 offset0:4 offset1:5
	ds_read2st64_b32 v[100:101], v118 offset0:6 offset1:7
	s_waitcnt lgkmcnt(3)
	v_add_f32_e32 v82, 0, v82
	v_add_f32_e32 v80, v82, v83
	s_waitcnt lgkmcnt(2)
	v_add_f32_e32 v80, v80, v86
	v_add_f32_e32 v80, v80, v87
	s_waitcnt lgkmcnt(1)
	v_add_f32_e32 v80, v80, v92
	v_add_f32_e32 v80, v80, v93
	s_waitcnt lgkmcnt(0)
	v_add_f32_e32 v80, v80, v100
	v_add_f32_e32 v80, v80, v101
	v_mul_f32_e32 v80, 0x3fb8aa3b, v80
	v_exp_f32_e32 v94, v80
	s_cbranch_vccnz .LBB0_1085
	ds_write_b32 v119, v94
.LBB0_1085:
	v_readlane_b32 s14, v255, 14
	v_readlane_b32 s15, v255, 15
	v_lshlrev_b32_e32 v189, 16, v90
	v_lshlrev_b32_e32 v109, 16, v97
	v_cndmask_b32_e64 v82, 0, v82, s[14:15]
	v_readlane_b32 s14, v255, 16
	v_readlane_b32 s15, v255, 17
	v_lshlrev_b32_e32 v97, 16, v186
	v_add_u32_e32 v194, s90, v120
	v_cndmask_b32_e64 v83, 0, v83, s[14:15]
	v_readlane_b32 s14, v255, 18
	v_readlane_b32 s15, v255, 19
	v_add_f32_e32 v82, v82, v83
	v_lshlrev_b32_e32 v104, 16, v95
	v_cndmask_b32_e64 v83, 0, v86, s[14:15]
	v_readlane_b32 s14, v255, 20
	v_readlane_b32 s15, v255, 21
	v_add_f32_e32 v82, v82, v83
	v_lshlrev_b32_e32 v95, 16, v96
	v_cndmask_b32_e64 v83, 0, v87, s[14:15]
	v_readlane_b32 s14, v255, 22
	v_readlane_b32 s15, v255, 23
	v_add_f32_e32 v82, v82, v83
	v_lshlrev_b32_e32 v190, 16, v99
	v_cndmask_b32_e64 v83, 0, v92, s[14:15]
	v_readlane_b32 s14, v255, 24
	v_readlane_b32 s15, v255, 25
	v_lshl_add_u64 v[244:245], v[244:245], 0, v[246:247]
	global_load_dwordx4 v[6:9], v[244:245], off
	v_add_f32_e32 v82, v82, v83
	v_lshlrev_b32_e32 v96, 16, v113
	v_cndmask_b32_e64 v83, 0, v93, s[14:15]
	v_readlane_b32 s14, v255, 26
	v_readlane_b32 s15, v255, 27
	v_add_f32_e32 v82, v82, v83
	v_lshlrev_b32_e32 v113, 16, v114
	v_cndmask_b32_e64 v83, 0, v100, s[14:15]
	v_readlane_b32 s14, v255, 28
	v_readlane_b32 s15, v255, 29
	v_add_f32_e32 v82, v82, v83
	v_lshlrev_b32_e32 v105, 16, v102
	v_cndmask_b32_e64 v83, 0, v101, s[14:15]
; #define LAS __attribute__((address_space(3)))
; __device__ __forceinline__ unsigned f2bf(float f) { unsigned u = __builtin_bit_cast(unsigned, f); return (u + 0x7fffu + ((u >> 16) & 1u)) >> 16; }
; __device__ __forceinline__ void p4a_chunk(Frame& F0, const In& I) {
;     ...
;         float at_[8], bh_[8], kh_[8]; const float gtot = __expf(tot); float ep_prev = 1.f;
; #pragma unroll
;         for (int i = 0; i < 8; ++i) { const int t = 8 * w + i; const float cum = pre + cs[i], cump = cum - lwv[i];
;             const float kkv = kk[i] * kkp; const float n2 = wave_sum(kkv * kkv); const float kkn = kkv * __builtin_amdgcn_rsqf(fmaxf(n2, 1e-24f));
;             const float a = -kkn, bb = kkn * ic[i], kp = kk[i] * (1.0f + (ic[i] - 1.0f) * kap);
;             const float ep = __expf(cum), em = __builtin_amdgcn_rcpf(ep), epp = (i == 0) ? __expf(cump) : ep_prev, eL = gtot * em; ep_prev = ep;
;             const float Rv = rr[i] * ep, Av = a * epp, Bv = bb * em, Kv = kp * em;
;             at_[i] = Av; bh_[i] = bb * eL; kh_[i] = kp * eL;
;             *(LAS unsigned short*)(L + C_RT + t * CP + lane * 2) = (unsigned short)f2bf(Rv);
;             *(LAS unsigned short*)(L + C_AT + t * CP + lane * 2) = (unsigned short)f2bf(Av);
;             *(LAS unsigned short*)(L + C_BT + t * CP + lane * 2) = (unsigned short)f2bf(Bv);
;             *(LAS unsigned short*)(L + C_KT + t * CP + lane * 2) = (unsigned short)f2bf(Kv); }
	v_add_f32_e32 v193, v82, v83
	v_add_f32_e32 v83, v187, v193
	v_mul_f32_e32 v82, 0x3fb8aa3b, v83
	v_exp_f32_e32 v82, v82
	v_sub_f32_e32 v83, v83, v89
	v_mul_f32_e32 v83, 0x3fb8aa3b, v83
	v_exp_f32_e32 v186, v83
	v_mul_f32_e32 v83, v82, v189
	v_bfe_u32 v89, v83, 16, 1
	v_add3_u32 v83, v83, v89, s3
	v_add_f32_e32 v89, v185, v193
	v_mul_f32_e32 v89, 0x3fb8aa3b, v89
	v_exp_f32_e32 v187, v89
	ds_write_b16_d16_hi v194, v83
	v_add_f32_e32 v83, v184, v193
	v_mul_f32_e32 v83, 0x3fb8aa3b, v83
	v_mul_f32_e32 v89, v187, v95
	v_exp_f32_e32 v83, v83
	v_bfe_u32 v95, v89, 16, 1
	v_add3_u32 v89, v89, v95, s3
	v_add_f32_e32 v95, v183, v193
	v_mul_f32_e32 v95, 0x3fb8aa3b, v95
	v_exp_f32_e32 v114, v95
	ds_write_b16_d16_hi v194, v89 offset:144
	v_mul_f32_e32 v89, v83, v190
	v_add_f32_e32 v100, v181, v193
	v_bfe_u32 v95, v89, 16, 1
	v_mul_f32_e32 v100, 0x3fb8aa3b, v100
	v_lshlrev_b32_e32 v102, 16, v106
	v_lshlrev_b32_e32 v80, 16, v85
	v_lshlrev_b32_e32 v85, 16, v103
	v_lshlrev_b32_e32 v103, 16, v112
	v_add3_u32 v89, v89, v95, s3
	v_exp_f32_e32 v112, v100
	ds_write_b16_d16_hi v194, v89 offset:288
	v_mul_f32_e32 v89, v114, v102
	v_add_f32_e32 v101, v180, v193
	v_bfe_u32 v95, v89, 16, 1
	v_mul_f32_e32 v101, 0x3fb8aa3b, v101
	v_lshlrev_b32_e32 v108, 16, v84
	v_lshlrev_b32_e32 v84, 16, v91
	v_lshl_add_u64 v[244:245], v[244:245], 0, v[246:247]
	global_load_dwordx4 v[10:13], v[244:245], off
	v_lshlrev_b32_e32 v91, 16, v115
	v_add3_u32 v89, v89, v95, s3
	v_exp_f32_e32 v115, v101
	ds_write_b16_d16_hi v194, v89 offset:432
	v_mul_f32_e32 v89, v112, v103
	v_bfe_u32 v95, v89, 16, 1
	v_add3_u32 v89, v89, v95, s3
	v_add_f32_e32 v95, v179, v193
	ds_write_b16_d16_hi v194, v89 offset:576
	v_mul_f32_e32 v89, v115, v113
	v_mul_f32_e32 v95, 0x3fb8aa3b, v95
	v_exp_f32_e32 v113, v95
	v_bfe_u32 v95, v89, 16, 1
	v_add3_u32 v89, v89, v95, s3
	v_add_f32_e32 v95, v178, v193
	v_mul_f32_e32 v95, 0x3fb8aa3b, v95
	v_lshlrev_b32_e32 v191, 16, v177
	v_exp_f32_e32 v95, v95
	ds_write_b16_d16_hi v194, v89 offset:720
	v_mul_f32_e32 v89, v113, v191
	v_bfe_u32 v103, v89, 16, 1
	v_lshlrev_b32_e32 v192, 16, v188
	v_add3_u32 v89, v89, v103, s3
	v_lshlrev_b32_e32 v81, 16, v98
	ds_write_b16_d16_hi v194, v89 offset:864
	v_mul_f32_e32 v89, v95, v192
	v_pk_mul_f32 v[178:179], v[88:89], v[80:81] op_sel_hi:[0,1]
	v_pk_mul_f32 v[180:181], v[178:179], v[178:179]
	v_rcp_f32_e32 v103, v95
	v_lshlrev_b32_e32 v93, 16, v182
	v_add_f32_dpp v95, v180, v180 quad_perm:[1,0,3,2] row_mask:0xf bank_mask:0xf bound_ctrl:1
	v_rcp_f32_e32 v182, v187
	v_lshlrev_b32_e32 v99, 16, v176
	v_add_f32_dpp v95, v95, v95 quad_perm:[2,3,0,1] row_mask:0xf bank_mask:0xf bound_ctrl:1
	v_rcp_f32_e32 v176, v82
	v_rcp_f32_e32 v177, v83
	v_add_f32_dpp v95, v95, v95 row_ror:4 row_mask:0xf bank_mask:0xf bound_ctrl:1
	v_pk_add_f32 v[86:87], v[108:109], -1.0 op_sel_hi:[1,0]
	v_pk_add_f32 v[188:189], v[104:105], -1.0 op_sel_hi:[1,0]
	v_add_f32_dpp v95, v95, v95 row_ror:8 row_mask:0xf bank_mask:0xf bound_ctrl:1
	v_rcp_f32_e32 v183, v114
	v_readlane_b32 s16, v95, 16
	v_readlane_b32 s17, v95, 48
	v_readlane_b32 s14, v95, 0
	v_readlane_b32 s15, v95, 32
	v_mov_b32_e32 v184, s16
	v_mov_b32_e32 v185, s17
	v_pk_add_f32 v[184:185], s[14:15], v[184:185]
	v_lshlrev_b32_e32 v90, 16, v107
	v_add_f32_e32 v95, v184, v185
	v_max_f32_e32 v95, 0x179abe15, v95
	v_rsq_f32_e32 v180, v95
	v_lshl_add_u64 v[244:245], v[244:245], 0, v[246:247]
	global_load_dwordx4 v[14:17], v[244:245], off
	v_rcp_f32_e32 v102, v115
	v_add_f32_dpp v95, v181, v181 quad_perm:[1,0,3,2] row_mask:0xf bank_mask:0xf bound_ctrl:1
	v_lshlrev_b32_e32 v92, 16, v111
	v_lshlrev_b32_e32 v98, 16, v110
	v_add_f32_dpp v95, v95, v95 quad_perm:[2,3,0,1] row_mask:0xf bank_mask:0xf bound_ctrl:1
	v_rcp_f32_e32 v100, v112
	v_pk_add_f32 v[106:107], v[98:99], -1.0 op_sel_hi:[1,0]
	v_add_f32_dpp v95, v95, v95 row_ror:4 row_mask:0xf bank_mask:0xf bound_ctrl:1
	v_rcp_f32_e32 v101, v113
	v_pk_add_f32 v[110:111], v[96:97], -1.0 op_sel_hi:[1,0]
	v_add_f32_dpp v95, v95, v95 row_ror:8 row_mask:0xf bank_mask:0xf bound_ctrl:1
	s_cmp_lt_i32 s85, 0x18000
	v_readlane_b32 s16, v95, 16
	v_readlane_b32 s17, v95, 48
	v_readlane_b32 s14, v95, 0
	v_readlane_b32 s15, v95, 32
	v_mov_b32_e32 v184, s16
	v_mov_b32_e32 v185, s17
	v_pk_add_f32 v[184:185], s[14:15], v[184:185]
	s_cselect_b64 s[74:75], -1, 0
	v_add_f32_e32 v95, v184, v185
	v_max_f32_e32 v95, 0x179abe15, v95
	v_rsq_f32_e32 v181, v95
	v_bfe_u32 v95, v89, 16, 1
	v_add3_u32 v89, v89, v95, s3
	ds_write_b16_d16_hi v194, v89 offset:1008
	v_pk_mul_f32 v[178:179], v[178:179], v[180:181]
	s_mov_b64 s[64:65], -1
	v_pk_mul_f32 v[180:181], v[186:187], v[178:179] neg_lo:[0,1] neg_hi:[0,1]
	v_pk_mul_f32 v[108:109], v[178:179], v[108:109]
	v_and_b32_sdwa v89, v181, v159 dst_sel:DWORD dst_unused:UNUSED_PAD src0_sel:WORD_1 src1_sel:DWORD
	v_and_b32_sdwa v95, v180, v159 dst_sel:DWORD dst_unused:UNUSED_PAD src0_sel:WORD_1 src1_sel:DWORD
	v_add3_u32 v89, v181, v89, s3
	v_add3_u32 v95, v180, v95, s3
	v_pk_mul_f32 v[180:181], v[88:89], v[84:85] op_sel_hi:[0,1]
	v_pk_mul_f32 v[184:185], v[180:181], v[180:181]
	ds_write_b16_d16_hi v194, v95 offset:55296
	s_nop 0
	v_add_f32_dpp v184, v184, v184 quad_perm:[1,0,3,2] row_mask:0xf bank_mask:0xf bound_ctrl:1
	v_add_f32_dpp v185, v185, v185 quad_perm:[1,0,3,2] row_mask:0xf bank_mask:0xf bound_ctrl:1
	s_nop 0
	v_add_f32_dpp v184, v184, v184 quad_perm:[2,3,0,1] row_mask:0xf bank_mask:0xf bound_ctrl:1
	v_add_f32_dpp v185, v185, v185 quad_perm:[2,3,0,1] row_mask:0xf bank_mask:0xf bound_ctrl:1
	s_nop 0
	v_add_f32_dpp v184, v184, v184 row_ror:4 row_mask:0xf bank_mask:0xf bound_ctrl:1
	v_add_f32_dpp v185, v185, v185 row_ror:4 row_mask:0xf bank_mask:0xf bound_ctrl:1
; #define LAS __attribute__((address_space(3)))
; __device__ __forceinline__ unsigned f2bf(float f) { unsigned u = __builtin_bit_cast(unsigned, f); return (u + 0x7fffu + ((u >> 16) & 1u)) >> 16; }
; __device__ __forceinline__ void p4a_chunk(Frame& F0, const In& I) {
;     ...
;         for (int i = 0; i < 8; ++i) { const int t = 8 * w + i; const float cum = pre + cs[i], cump = cum - lwv[i];
;             const float kkv = kk[i] * kkp; const float n2 = wave_sum(kkv * kkv); const float kkn = kkv * __builtin_amdgcn_rsqf(fmaxf(n2, 1e-24f));
;             const float a = -kkn, bb = kkn * ic[i], kp = kk[i] * (1.0f + (ic[i] - 1.0f) * kap);
;             const float ep = __expf(cum), em = __builtin_amdgcn_rcpf(ep), epp = (i == 0) ? __expf(cump) : ep_prev, eL = gtot * em; ep_prev = ep;
;             const float Rv = rr[i] * ep, Av = a * epp, Bv = bb * em, Kv = kp * em;
;             at_[i] = Av; bh_[i] = bb * eL; kh_[i] = kp * eL;
;             *(LAS unsigned short*)(L + C_RT + t * CP + lane * 2) = (unsigned short)f2bf(Rv);
;             *(LAS unsigned short*)(L + C_AT + t * CP + lane * 2) = (unsigned short)f2bf(Av);
;             *(LAS unsigned short*)(L + C_BT + t * CP + lane * 2) = (unsigned short)f2bf(Bv);
;             *(LAS unsigned short*)(L + C_KT + t * CP + lane * 2) = (unsigned short)f2bf(Kv); }
	s_nop 0
	v_add_f32_dpp v184, v184, v184 row_ror:8 row_mask:0xf bank_mask:0xf bound_ctrl:1
	v_add_f32_dpp v185, v185, v185 row_ror:8 row_mask:0xf bank_mask:0xf bound_ctrl:1
	v_readlane_b32 s16, v184, 16
	v_readlane_b32 s17, v184, 48
	v_readlane_b32 s14, v184, 0
	v_readlane_b32 s15, v184, 32
	v_mov_b32_e32 v186, s16
	v_lshl_add_u64 v[244:245], v[244:245], 0, v[246:247]
	global_load_dwordx4 v[18:21], v[244:245], off
	v_mov_b32_e32 v187, s17
	v_pk_add_f32 v[186:187], s[14:15], v[186:187]
	v_readlane_b32 s16, v185, 16
	v_readlane_b32 s17, v185, 48
	v_add_f32_e32 v184, v186, v187
	v_readlane_b32 s14, v185, 0
	v_readlane_b32 s15, v185, 32
	v_mov_b32_e32 v186, s16
	v_mov_b32_e32 v187, s17
	v_pk_add_f32 v[186:187], s[14:15], v[186:187]
	v_max_f32_e32 v184, 0x179abe15, v184
	v_add_f32_e32 v185, v186, v187
	v_max_f32_e32 v185, 0x179abe15, v185
	v_rsq_f32_e32 v184, v184
	v_rsq_f32_e32 v185, v185
	v_lshrrev_b32_e32 v186, 16, v95
	v_lshrrev_b32_e32 v187, 16, v89
	v_pk_mul_f32 v[180:181], v[180:181], v[184:185]
	s_nop 0
	v_pk_mul_f32 v[82:83], v[82:83], v[180:181] neg_lo:[0,1] neg_hi:[0,1]
	v_pk_mul_f32 v[104:105], v[180:181], v[104:105]
	v_and_b32_sdwa v95, v83, v159 dst_sel:DWORD dst_unused:UNUSED_PAD src0_sel:WORD_1 src1_sel:DWORD
	v_and_b32_sdwa v184, v82, v159 dst_sel:DWORD dst_unused:UNUSED_PAD src0_sel:WORD_1 src1_sel:DWORD
	v_add3_u32 v185, v83, v95, s3
	v_add3_u32 v184, v82, v184, s3
	v_pk_fma_f32 v[82:83], v[86:87], v[68:69], 1.0 op_sel_hi:[1,0,0]
	ds_write_b16_d16_hi v194, v184 offset:55440
	ds_write_b16_d16_hi v194, v89 offset:55584
	ds_write_b16_d16_hi v194, v185 offset:55728
	v_pk_mul_f32 v[80:81], v[82:83], v[80:81]
	v_pk_mul_f32 v[82:83], v[94:95], v[176:177] op_sel_hi:[0,1]
	v_mul_f32_e32 v86, v80, v176
	v_bfe_u32 v87, v86, 16, 1
	v_add3_u32 v86, v86, v87, s3
	ds_write_b16_d16_hi v71, v86
	v_pk_fma_f32 v[86:87], v[188:189], v[68:69], 1.0 op_sel_hi:[1,0,0]
	s_nop 0
	v_pk_mul_f32 v[84:85], v[86:87], v[84:85]
	v_pk_mul_f32 v[86:87], v[94:95], v[182:183] op_sel_hi:[0,1]
	v_mul_f32_e32 v89, v84, v182
	v_bfe_u32 v95, v89, 16, 1
	v_add3_u32 v89, v89, v95, s3
	ds_write_b16_d16_hi v71, v89 offset:144
	v_mul_f32_e32 v89, v81, v177
	v_bfe_u32 v95, v89, 16, 1
	v_add3_u32 v89, v89, v95, s3
	ds_write_b16_d16_hi v71, v89 offset:288
	v_mul_f32_e32 v89, v85, v183
	v_bfe_u32 v95, v89, 16, 1
	v_add3_u32 v89, v89, v95, s3
	ds_write_b16_d16_hi v71, v89 offset:432
	v_mul_f32_e32 v89, v176, v108
	v_bfe_u32 v95, v89, 16, 1
	v_lshl_add_u64 v[244:245], v[244:245], 0, v[246:247]
	global_load_dwordx4 v[22:25], v[244:245], off
	v_add3_u32 v89, v89, v95, s3
	ds_write_b16_d16_hi v194, v89 offset:64512
	v_mul_f32_e32 v89, v182, v104
	v_bfe_u32 v95, v89, 16, 1
	v_add3_u32 v89, v89, v95, s3
	ds_write_b16_d16_hi v194, v89 offset:64656
	v_mul_f32_e32 v89, v177, v109
	v_bfe_u32 v95, v89, 16, 1
	v_add3_u32 v89, v89, v95, s3
	ds_write_b16_d16_hi v194, v89 offset:64800
	v_mul_f32_e32 v89, v183, v105
	v_bfe_u32 v95, v89, 16, 1
	v_add3_u32 v89, v89, v95, s3
	v_pk_mul_f32 v[176:177], v[88:89], v[90:91] op_sel_hi:[0,1]
	v_pk_mul_f32 v[178:179], v[176:177], v[176:177]
	ds_write_b16_d16_hi v194, v89 offset:64944
	v_pk_mul_f32 v[104:105], v[86:87], v[104:105]
	v_add_f32_dpp v95, v178, v178 quad_perm:[1,0,3,2] row_mask:0xf bank_mask:0xf bound_ctrl:1
	v_pk_mul_f32 v[108:109], v[82:83], v[108:109]
	s_nop 0
	v_add_f32_dpp v95, v95, v95 quad_perm:[2,3,0,1] row_mask:0xf bank_mask:0xf bound_ctrl:1
	s_nop 1
	v_add_f32_dpp v95, v95, v95 row_ror:4 row_mask:0xf bank_mask:0xf bound_ctrl:1
	s_nop 1
	v_add_f32_dpp v95, v95, v95 row_ror:8 row_mask:0xf bank_mask:0xf bound_ctrl:1
	s_nop 0
	v_readlane_b32 s16, v95, 16
	v_readlane_b32 s17, v95, 48
	v_readlane_b32 s14, v95, 0
	v_readlane_b32 s15, v95, 32
	v_mov_b32_e32 v180, s16
	v_mov_b32_e32 v181, s17
	v_pk_add_f32 v[180:181], s[14:15], v[180:181]
	s_nop 0
	v_add_f32_e32 v95, v180, v181
	v_max_f32_e32 v95, 0x179abe15, v95
	v_rsq_f32_e32 v178, v95
	s_nop 0
	v_add_f32_dpp v95, v179, v179 quad_perm:[1,0,3,2] row_mask:0xf bank_mask:0xf bound_ctrl:1
	s_nop 1
	v_add_f32_dpp v95, v95, v95 quad_perm:[2,3,0,1] row_mask:0xf bank_mask:0xf bound_ctrl:1
	s_nop 1
	v_add_f32_dpp v95, v95, v95 row_ror:4 row_mask:0xf bank_mask:0xf bound_ctrl:1
	s_nop 1
	v_add_f32_dpp v95, v95, v95 row_ror:8 row_mask:0xf bank_mask:0xf bound_ctrl:1
	s_nop 0
	v_readlane_b32 s16, v95, 16
	v_readlane_b32 s17, v95, 48
	v_readlane_b32 s14, v95, 0
	v_readlane_b32 s15, v95, 32
	v_mov_b32_e32 v180, s16
	v_mov_b32_e32 v181, s17
	v_pk_add_f32 v[180:181], s[14:15], v[180:181]
	s_nop 0
	v_add_f32_e32 v95, v180, v181
	v_lshl_add_u64 v[244:245], v[244:245], 0, v[246:247]
	global_load_dwordx4 v[26:29], v[244:245], off
	v_max_f32_e32 v95, 0x179abe15, v95
	v_rsq_f32_e32 v179, v95
	s_nop 0
	v_pk_mul_f32 v[176:177], v[176:177], v[178:179]
	s_nop 0
	v_pk_mul_f32 v[114:115], v[114:115], v[176:177] neg_lo:[0,1] neg_hi:[0,1]
	v_pk_mul_f32 v[98:99], v[176:177], v[98:99]
	v_and_b32_sdwa v89, v115, v159 dst_sel:DWORD dst_unused:UNUSED_PAD src0_sel:WORD_1 src1_sel:DWORD
	v_and_b32_sdwa v95, v114, v159 dst_sel:DWORD dst_unused:UNUSED_PAD src0_sel:WORD_1 src1_sel:DWORD
	v_add3_u32 v180, v115, v89, s3
	v_pk_mul_f32 v[88:89], v[88:89], v[92:93] op_sel_hi:[0,1]
	v_add3_u32 v95, v114, v95, s3
; #define LAS __attribute__((address_space(3)))
; __device__ __forceinline__ unsigned f2bf(float f) { unsigned u = __builtin_bit_cast(unsigned, f); return (u + 0x7fffu + ((u >> 16) & 1u)) >> 16; }
; __device__ __forceinline__ unsigned pk2(float lo, float hi) { return f2bf(lo) | (f2bf(hi) << 16); }
; #define CBAR() do { asm volatile("s_waitcnt lgkmcnt(0)" ::: "memory"); __builtin_amdgcn_s_barrier(); asm volatile("" ::: "memory"); } while (0)
; __device__ __forceinline__ void p4a_chunk(Frame& F0, const In& I) {
;     ...
;         for (int i = 0; i < 8; ++i) { const int t = 8 * w + i; const float cum = pre + cs[i], cump = cum - lwv[i];
;             const float kkv = kk[i] * kkp; const float n2 = wave_sum(kkv * kkv); const float kkn = kkv * __builtin_amdgcn_rsqf(fmaxf(n2, 1e-24f));
;             const float a = -kkn, bb = kkn * ic[i], kp = kk[i] * (1.0f + (ic[i] - 1.0f) * kap);
;             const float ep = __expf(cum), em = __builtin_amdgcn_rcpf(ep), epp = (i == 0) ? __expf(cump) : ep_prev, eL = gtot * em; ep_prev = ep;
;             const float Rv = rr[i] * ep, Av = a * epp, Bv = bb * em, Kv = kp * em;
;             at_[i] = Av; bh_[i] = bb * eL; kh_[i] = kp * eL;
;             *(LAS unsigned short*)(L + C_RT + t * CP + lane * 2) = (unsigned short)f2bf(Rv);
;             *(LAS unsigned short*)(L + C_AT + t * CP + lane * 2) = (unsigned short)f2bf(Av);
;             *(LAS unsigned short*)(L + C_BT + t * CP + lane * 2) = (unsigned short)f2bf(Bv);
;             *(LAS unsigned short*)(L + C_KT + t * CP + lane * 2) = (unsigned short)f2bf(Kv); }
; #pragma unroll
;         for (int q = 0; q < 4; ++q) { att[q] = pk2(at_[2 * q], at_[2 * q + 1]); bht[q] = pk2(bh_[2 * q], bh_[2 * q + 1]); kht[q] = pk2(kh_[2 * q], kh_[2 * q + 1]); vtt[q] = pk2(vv[2 * q], vv[2 * q + 1]); }
;         *(LAS v4u*)(L + C_ATT + lane * CP + 16 * w) = (v4u){att[0], att[1], att[2], att[3]};
;         *(LAS v4u*)(L + C_WA + (64 + lane) * CP + 16 * w) = (v4u){bht[0], bht[1], bht[2], bht[3]};
;         CBAR();
;         const int cit = unit * 12 + w; const bool hx = cit < MOE_NITEMS, hy = (w < 4) && (cit + 8 < MOE_NITEMS);
;         f32x4 tX[16]; MoeItem mX = moe_item(hx ? cit : 0, I.w_gu, I.w_down, F.ws);
	v_pk_mul_f32 v[114:115], v[88:89], v[88:89]
	ds_write_b16_d16_hi v194, v95 offset:55872
	s_nop 0
	v_add_f32_dpp v114, v114, v114 quad_perm:[1,0,3,2] row_mask:0xf bank_mask:0xf bound_ctrl:1
	v_add_f32_dpp v115, v115, v115 quad_perm:[1,0,3,2] row_mask:0xf bank_mask:0xf bound_ctrl:1
	s_nop 0
	v_add_f32_dpp v114, v114, v114 quad_perm:[2,3,0,1] row_mask:0xf bank_mask:0xf bound_ctrl:1
	v_add_f32_dpp v115, v115, v115 quad_perm:[2,3,0,1] row_mask:0xf bank_mask:0xf bound_ctrl:1
	s_nop 0
	v_add_f32_dpp v114, v114, v114 row_ror:4 row_mask:0xf bank_mask:0xf bound_ctrl:1
	v_add_f32_dpp v115, v115, v115 row_ror:4 row_mask:0xf bank_mask:0xf bound_ctrl:1
	s_nop 0
	v_add_f32_dpp v114, v114, v114 row_ror:8 row_mask:0xf bank_mask:0xf bound_ctrl:1
	v_add_f32_dpp v115, v115, v115 row_ror:8 row_mask:0xf bank_mask:0xf bound_ctrl:1
	v_readlane_b32 s16, v114, 16
	v_readlane_b32 s17, v114, 48
	v_readlane_b32 s14, v114, 0
	v_readlane_b32 s15, v114, 32
	v_mov_b32_e32 v178, s16
	v_mov_b32_e32 v179, s17
	v_pk_add_f32 v[178:179], s[14:15], v[178:179]
	v_readlane_b32 s16, v115, 16
	v_readlane_b32 s17, v115, 48
	v_add_f32_e32 v114, v178, v179
	v_readlane_b32 s14, v115, 0
	v_readlane_b32 s15, v115, 32
	v_mov_b32_e32 v178, s16
	v_mov_b32_e32 v179, s17
	v_pk_add_f32 v[178:179], s[14:15], v[178:179]
	v_max_f32_e32 v114, 0x179abe15, v114
	v_add_f32_e32 v115, v178, v179
	v_max_f32_e32 v115, 0x179abe15, v115
	v_rsq_f32_e32 v114, v114
	v_rsq_f32_e32 v115, v115
	v_lshrrev_b32_e32 v178, 16, v95
	v_lshrrev_b32_e32 v179, 16, v180
	s_and_b64 s[14:15], s[74:75], exec
	v_pk_mul_f32 v[114:115], v[88:89], v[114:115]
	s_cselect_b32 s15, s85, 0
	v_pk_mul_f32 v[88:89], v[112:113], v[114:115] neg_lo:[0,1] neg_hi:[0,1]
	v_pk_mul_f32 v[96:97], v[114:115], v[96:97]
	v_lshl_add_u64 v[244:245], v[244:245], 0, v[246:247]
	global_load_dwordx4 v[30:33], v[244:245], off
	v_and_b32_sdwa v95, v89, v159 dst_sel:DWORD dst_unused:UNUSED_PAD src0_sel:WORD_1 src1_sel:DWORD
	v_and_b32_sdwa v112, v88, v159 dst_sel:DWORD dst_unused:UNUSED_PAD src0_sel:WORD_1 src1_sel:DWORD
	v_add3_u32 v113, v89, v95, s3
	v_add3_u32 v112, v88, v112, s3
	v_pk_fma_f32 v[88:89], v[106:107], v[68:69], 1.0 op_sel_hi:[1,0,0]
	ds_write_b16_d16_hi v194, v112 offset:56016
	ds_write_b16_d16_hi v194, v180 offset:56160
	ds_write_b16_d16_hi v194, v113 offset:56304
	v_pk_mul_f32 v[88:89], v[88:89], v[90:91]
	s_cmp_gt_i32 s15, 0xffff
	v_mul_f32_e32 v95, v88, v100
	v_bfe_u32 v106, v95, 16, 1
	v_pk_mul_f32 v[90:91], v[94:95], v[100:101] op_sel_hi:[0,1]
	v_add3_u32 v95, v95, v106, s3
	v_pk_fma_f32 v[106:107], v[110:111], v[68:69], 1.0 op_sel_hi:[1,0,0]
	ds_write_b16_d16_hi v71, v95 offset:576
	v_pk_mul_f32 v[92:93], v[106:107], v[92:93]
	v_pk_mul_f32 v[94:95], v[94:95], v[102:103] op_sel_hi:[0,1]
	v_mul_f32_e32 v68, v92, v102
	v_bfe_u32 v106, v68, 16, 1
	v_add3_u32 v68, v68, v106, s3
	ds_write_b16_d16_hi v71, v68 offset:720
	v_mul_f32_e32 v68, v89, v101
	v_bfe_u32 v106, v68, 16, 1
	v_add3_u32 v68, v68, v106, s3
	ds_write_b16_d16_hi v71, v68 offset:864
	v_mul_f32_e32 v68, v93, v103
	v_bfe_u32 v106, v68, 16, 1
	v_add3_u32 v68, v68, v106, s3
	ds_write_b16_d16_hi v71, v68 offset:1008
	v_mul_f32_e32 v68, v100, v98
	v_bfe_u32 v100, v68, 16, 1
	v_add3_u32 v68, v68, v100, s3
	ds_write_b16_d16_hi v194, v68 offset:65088
	v_mul_f32_e32 v68, v102, v96
	v_bfe_u32 v100, v68, 16, 1
	v_add3_u32 v68, v68, v100, s3
	ds_write_b16_d16_hi v194, v68 offset:65232
	v_mul_f32_e32 v68, v101, v99
	v_bfe_u32 v100, v68, 16, 1
	v_add3_u32 v68, v68, v100, s3
	ds_write_b16_d16_hi v194, v68 offset:65376
	v_mul_f32_e32 v68, v103, v97
	v_bfe_u32 v100, v68, 16, 1
	v_add3_u32 v68, v68, v100, s3
	v_pk_mul_f32 v[100:101], v[90:91], v[98:99]
	v_pk_mul_f32 v[102:103], v[94:95], v[96:97]
	v_and_or_b32 v99, v113, s4, v179
	v_and_or_b32 v98, v112, s4, v178
	v_and_or_b32 v97, v185, s4, v187
	v_and_or_b32 v96, v184, s4, v186
	ds_write_b16_d16_hi v194, v68 offset:65520
	ds_write_b128 v73, v[96:99] offset:9216
	v_bfe_u32 v68, v103, 16, 1
	v_lshl_add_u64 v[244:245], v[244:245], 0, v[246:247]
	global_load_dwordx4 v[34:37], v[244:245], off
	v_bfe_u32 v96, v102, 16, 1
	v_bfe_u32 v98, v104, 16, 1
	v_add3_u32 v104, v104, v98, s3
	v_add3_u32 v96, v102, v96, s3
	v_add3_u32 v68, v103, v68, s3
	v_bfe_u32 v98, v108, 16, 1
	v_bfe_u32 v99, v109, 16, 1
	v_bfe_u32 v102, v100, 16, 1
	v_bfe_u32 v103, v101, 16, 1
	v_bfe_u32 v97, v105, 16, 1
	v_add3_u32 v101, v101, v103, s3
	v_add3_u32 v100, v100, v102, s3
	v_add3_u32 v99, v109, v99, s3
	v_add3_u32 v98, v108, v98, s3
	v_add3_u32 v97, v105, v97, s3
	v_lshrrev_b32_e32 v102, 16, v98
	v_lshrrev_b32_e32 v103, 16, v99
	v_lshrrev_b32_e32 v98, 16, v100
	v_lshrrev_b32_e32 v99, 16, v101
	v_and_or_b32 v99, v68, s4, v99
	v_and_or_b32 v98, v96, s4, v98
	v_and_or_b32 v97, v97, s4, v103
	v_and_or_b32 v96, v104, s4, v102
	ds_write_b128 v73, v[96:99] offset:46080
	s_waitcnt lgkmcnt(0)
	s_barrier
	s_cbranch_scc0 .LBB0_1087
	s_add_i32 s14, s15, 0xffff0000
	s_lshr_b32 s86, s14, 10
	s_bfe_u32 s14, s15, 0x50005
	s_lshl_b64 s[64:65], s[86:87], 22
	s_lshl_b32 s16, s14, 17
	s_lshl_b32 s17, s15, 6
	s_and_b32 s86, s17, 0x7c0
	s_or_b32 s16, s16, s64
	s_or_b32 s16, s16, s86
	s_add_u32 s72, s68, s64
	s_addc_u32 s73, s69, s65
	s_mov_b64 s[64:65], 0

; #define LAS __attribute__((address_space(3)))
; __device__ __forceinline__ unsigned f2bf(float f) { unsigned u = __builtin_bit_cast(unsigned, f); return (u + 0x7fffu + ((u >> 16) & 1u)) >> 16; }
; #define CBAR() do { asm volatile("s_waitcnt lgkmcnt(0)" ::: "memory"); __builtin_amdgcn_s_barrier(); asm volatile("" ::: "memory"); } while (0)
; __device__ __forceinline__ v2u pack4(const f32x4& v) { return (v2u){pg8::cvt_pk_bf16(v[0], v[1]), pg8::cvt_pk_bf16(v[2], v[3])}; }
; __device__ __forceinline__ void p4a_chunk(Frame& F0, const In& I) {
;     ...
;         const int nt = w & 3, mt0 = 2 * (w >> 2), n = nt * 16 + lr;
;         { const Fr yAT = LD(C_AT, nt), yKT = LD(C_KT, nt), yRT = LD(C_RT, nt);
;           Fr xBT[2], xAT[2], xKT[2];
; #pragma unroll
;           for (int i = 0; i < 2; ++i) { xBT[i] = LD(C_BT, mt0 + i); xAT[i] = LD(C_AT, mt0 + i); xKT[i] = LD(C_KT, mt0 + i); }
;           f32x4 a1[2], a2[2], a3[2], a4[2];
; #pragma unroll
;           for (int i = 0; i < 2; ++i) { a1[i] = MM(xBT[i], yAT); a2[i] = MM(xAT[i], yKT); a3[i] = MM(xBT[i], yRT); a4[i] = MM(xKT[i], yRT); }
; #pragma unroll
;           for (int i = 0; i < 2; ++i) { const int m0 = (mt0 + i) * 16 + 4 * kq;
;               f32x4 v = a1[i];
; #pragma unroll
;               for (int e = 0; e < 4; ++e) { v[e] = (m0 + e < n) ? v[e] : 0.f; *(LAS unsigned short*)(L + C_MA + (m0 + e) * CP + n * 2) = (unsigned short)f2bf(v[e]); }
;               *(LAS v2u*)(L + C_MTA + n * CP + m0 * 2) = pack4(v);
;               v = a2[i];
; #pragma unroll
;               for (int e = 0; e < 4; ++e) v[e] = (n < m0 + e) ? v[e] : 0.f;
;               *(LAS v2u*)(L + C_AAK + n * CP + m0 * 2) = pack4(v);
;               v = a3[i];
; #pragma unroll
;               for (int e = 0; e < 4; ++e) v[e] = (m0 + e <= n) ? v[e] : 0.f;
;               *(LAS v2u*)(L + C_WA + n * CP + m0 * 2) = pack4(v);
;               v = a4[i];
; #pragma unroll
;               for (int e = 0; e < 4; ++e) v[e] = (m0 + e <= n) ? v[e] : 0.f;
;               *(LAS v2u*)(L + C_ARKT + n * CP + m0 * 2) = pack4(v); } }
;         CBAR();
;         if (hx) tr8_load(mX, tX, lane);
.LBB0_1090:
	v_add_u32_e32 v96, v124, v131
	ds_read_b128 v[98:101], v96 offset:64512
	ds_read_b128 v[102:105], v123 offset:55296
	ds_read_b128 v[106:109], v96 offset:55296
	ds_read_b128 v[110:113], v123 offset:55360
	ds_read_b128 v[176:179], v96 offset:64576
	ds_read_b128 v[184:187], v152
	ds_read_b128 v[188:191], v152 offset:64
	ds_read_b128 v[192:195], v96 offset:55360
	s_waitcnt lgkmcnt(6)
	v_mfma_f32_16x16x32_bf16 v[180:183], v[98:101], v[102:105], 0
	ds_read_b128 v[196:199], v123
	ds_read_b128 v[200:203], v123 offset:64
	v_add_u32_e32 v68, v125, v131
	v_add_u32_e32 v97, v124, v139
	s_waitcnt lgkmcnt(4)
	v_mfma_f32_16x16x32_bf16 v[106:109], v[106:109], v[184:187], 0
	s_mov_b64 s[92:93], s[20:21]
	v_readlane_b32 s20, v255, 30
	v_add_u32_e32 v115, v126, v140
	v_mfma_f32_16x16x32_bf16 v[180:183], v[176:179], v[110:113], v[180:183]
	v_readlane_b32 s21, v255, 31
	s_andn2_b64 vcc, exec, s[74:75]
	s_waitcnt lgkmcnt(1)
	v_mfma_f32_16x16x32_bf16 v[98:101], v[98:101], v[196:199], 0
	v_mfma_f32_16x16x32_bf16 v[106:109], v[192:195], v[188:191], v[106:109]
	ds_read_b128 v[192:195], v68
	v_lshl_add_u64 v[244:245], v[244:245], 0, v[246:247]
	global_load_dwordx4 v[38:41], v[244:245], off
	ds_read_b128 v[204:207], v68 offset:64
	ds_read_b128 v[208:211], v97 offset:64512
	ds_read_b128 v[212:215], v97 offset:64576
	v_add_u32_e32 v68, v125, v139
	s_waitcnt lgkmcnt(4)
	v_mfma_f32_16x16x32_bf16 v[176:179], v[176:179], v[200:203], v[98:101]
	s_nop 2
	ds_read_b128 v[98:101], v97 offset:55296
	ds_read_b128 v[216:219], v97 offset:55360
	ds_read_b128 v[220:223], v68
	ds_read_b128 v[224:227], v68 offset:64
	v_cndmask_b32_e64 v68, 0, v180, s[18:19]
	v_bfe_u32 v114, v68, 16, 1
	s_waitcnt lgkmcnt(5)
	v_mfma_f32_16x16x32_bf16 v[102:105], v[208:211], v[102:105], 0
	v_add3_u32 v114, v68, v114, s3
	ds_write_b16_d16_hi v115, v114
	v_cndmask_b32_e64 v114, 0, v181, s[20:21]
	v_bfe_u32 v180, v114, 16, 1
	v_readlane_b32 s20, v255, 32
	s_waitcnt lgkmcnt(5)
	v_mfma_f32_16x16x32_bf16 v[102:105], v[212:215], v[110:113], v[102:105]
	v_add3_u32 v110, v114, v180, s3
	v_readlane_b32 s21, v255, 33
	ds_write_b16_d16_hi v115, v110 offset:144
	s_waitcnt lgkmcnt(5)
	v_mfma_f32_16x16x32_bf16 v[98:101], v[98:101], v[184:187], 0
	v_cndmask_b32_e64 v115, 0, v182, s[20:21]
	v_readlane_b32 s20, v255, 34
	v_bfe_u32 v110, v115, 16, 1
	v_readlane_b32 s21, v255, 35
	v_add3_u32 v110, v115, v110, s3
	ds_write_b16_d16_hi v153, v110
	v_cndmask_b32_e64 v180, 0, v183, s[20:21]
	s_waitcnt lgkmcnt(5)
	v_mfma_f32_16x16x32_bf16 v[110:113], v[216:219], v[188:191], v[98:101]
	v_cvt_pk_bf16_f32 v114, v68, v114
	v_cvt_pk_bf16_f32 v115, v115, v180
	v_cndmask_b32_e64 v68, 0, v106, s[26:27]
	v_bfe_u32 v98, v180, 16, 1
	v_mfma_f32_16x16x32_bf16 v[192:195], v[192:195], v[196:199], 0
	v_add3_u32 v181, v180, v98, s3
	ds_write_b16_d16_hi v154, v181
	v_readlane_b32 s20, v255, 36
	v_mfma_f32_16x16x32_bf16 v[98:101], v[208:211], v[196:199], 0
	v_readlane_b32 s21, v255, 37
	v_mfma_f32_16x16x32_bf16 v[192:195], v[204:207], v[200:203], v[192:195]
	v_mfma_f32_16x16x32_bf16 v[180:183], v[212:215], v[200:203], v[98:101]
	s_nop 4
	v_add_u32_e32 v99, v127, v141
	v_lshl_add_u64 v[244:245], v[244:245], 0, v[246:247]
	global_load_dwordx4 v[42:45], v[244:245], off
	ds_write_b64 v99, v[114:115]
	v_cndmask_b32_e64 v98, v107, 0, s[18:19]
	v_cndmask_b32_e64 v101, 0, v108, s[28:29]
	v_cndmask_b32_e64 v114, 0, v109, s[30:31]
	v_cvt_pk_bf16_f32 v100, v68, v98
	v_cvt_pk_bf16_f32 v101, v101, v114
	v_cndmask_b32_e64 v98, v176, 0, s[26:27]
	v_cndmask_b32_e64 v114, 0, v177, s[18:19]
	v_cndmask_b32_e64 v115, v178, 0, s[28:29]
	v_cndmask_b32_e64 v176, v179, 0, s[30:31]
	v_add_u32_e32 v68, v121, v141
	v_cvt_pk_bf16_f32 v114, v98, v114
	v_cvt_pk_bf16_f32 v115, v115, v176
	ds_write_b64 v68, v[114:115] offset:36864
	v_cndmask_b32_e64 v98, v192, 0, s[26:27]
	v_cndmask_b32_e64 v114, 0, v193, s[18:19]
	v_cndmask_b32_e64 v115, v194, 0, s[28:29]
	v_cndmask_b32_e64 v176, v195, 0, s[30:31]
	v_cvt_pk_bf16_f32 v114, v98, v114
	v_cvt_pk_bf16_f32 v115, v115, v176
	ds_write2st64_b64 v68, v[100:101], v[114:115] offset0:36 offset1:54
	v_cndmask_b32_e64 v68, 0, v102, s[34:35]
	v_bfe_u32 v98, v68, 16, 1
	v_add3_u32 v98, v68, v98, s3
	v_add_u32_e32 v100, v126, v142
	ds_write_b16_d16_hi v100, v98
	v_cndmask_b32_e64 v98, 0, v103, s[20:21]
	v_bfe_u32 v101, v98, 16, 1
	v_readlane_b32 s20, v255, 38
	v_add3_u32 v101, v98, v101, s3
	v_readlane_b32 s21, v255, 39
	ds_write_b16_d16_hi v100, v101 offset:144
	s_waitcnt lgkmcnt(10)
	v_mfma_f32_16x16x32_bf16 v[184:187], v[220:223], v[196:199], 0
	v_cndmask_b32_e64 v101, 0, v104, s[20:21]
	v_readlane_b32 s20, v255, 40
	v_bfe_u32 v100, v101, 16, 1
	v_readlane_b32 s21, v255, 41
	v_add3_u32 v100, v101, v100, s3
	ds_write_b16_d16_hi v155, v100
	v_cndmask_b32_e64 v102, 0, v105, s[20:21]
	v_bfe_u32 v100, v102, 16, 1
	v_add3_u32 v100, v102, v100, s3
	s_waitcnt lgkmcnt(10)
	v_mfma_f32_16x16x32_bf16 v[106:109], v[224:227], v[200:203], v[184:187]
	ds_write_b16_d16_hi v156, v100
	v_cvt_pk_bf16_f32 v100, v68, v98
	v_cvt_pk_bf16_f32 v101, v101, v102
	v_add_u32_e32 v98, v127, v143
	ds_write_b64 v98, v[100:101]
	v_lshl_add_u64 v[244:245], v[244:245], 0, v[246:247]
	global_load_dwordx4 v[46:49], v[244:245], off
	v_cndmask_b32_e64 v101, 0, v112, s[44:45]
	v_cndmask_b32_e64 v102, 0, v113, s[46:47]
	v_cndmask_b32_e64 v68, 0, v110, s[42:43]
	v_cndmask_b32_e64 v100, v111, 0, s[34:35]
	v_cvt_pk_bf16_f32 v101, v101, v102
	v_cndmask_b32_e64 v102, v180, 0, s[42:43]
	v_cndmask_b32_e64 v103, 0, v181, s[34:35]
	v_cndmask_b32_e64 v104, v182, 0, s[44:45]
	v_cndmask_b32_e64 v105, v183, 0, s[46:47]
	v_cvt_pk_bf16_f32 v100, v68, v100
	v_add_u32_e32 v68, v121, v143
	v_cvt_pk_bf16_f32 v102, v102, v103
	v_cvt_pk_bf16_f32 v103, v104, v105
	ds_write_b64 v68, v[102:103] offset:36864
	v_cndmask_b32_e64 v102, v106, 0, s[42:43]
	v_cndmask_b32_e64 v103, 0, v107, s[34:35]
	v_cndmask_b32_e64 v104, v108, 0, s[44:45]
	v_cndmask_b32_e64 v105, v109, 0, s[46:47]
	v_cvt_pk_bf16_f32 v102, v102, v103
	v_cvt_pk_bf16_f32 v103, v104, v105
	ds_write2st64_b64 v68, v[100:101], v[102:103] offset0:36 offset1:54
	s_waitcnt lgkmcnt(0)
	s_barrier
	v_cndmask_b32_e64 v68, 0, 1, s[74:75]
	v_cmp_ne_u32_e64 s[64:65], 1, v68
	s_cbranch_vccnz .LBB0_1092
	s_lshl_b32 s74, s16, 2
	s_add_i32 s16, s15, s16
	s_add_i32 s17, s15, s74
	s_lshl_b32 s16, s16, 2
	s_add_i32 s17, s17, s15
	s_add_i32 s17, s17, s15
	s_lshl_b32 s16, s15, 1
	s_add_i32 s16, s17, s16
	s_add_i32 s16, s16, s15
	s_add_i32 s16, s16, s15
	s_add_i32 s16, s16, s15
	s_add_i32 s16, s16, s15
	s_add_i32 s16, s16, s15
	s_add_i32 s16, s16, s15
	s_add_i32 s16, s16, s15
	s_add_i32 s16, s16, s15
	s_add_i32 s16, s16, s15
	s_add_i32 s16, s16, s15
; #define LAS __attribute__((address_space(3)))
; __device__ __forceinline__ unsigned f2bf(float f) { unsigned u = __builtin_bit_cast(unsigned, f); return (u + 0x7fffu + ((u >> 16) & 1u)) >> 16; }
; #define CBAR() do { asm volatile("s_waitcnt lgkmcnt(0)" ::: "memory"); __builtin_amdgcn_s_barrier(); asm volatile("" ::: "memory"); } while (0)
; __device__ __forceinline__ v2u pack4(const f32x4& v) { return (v2u){pg8::cvt_pk_bf16(v[0], v[1]), pg8::cvt_pk_bf16(v[2], v[3])}; }
; __device__ __forceinline__ void p4a_chunk(Frame& F0, const In& I) {
;     ...
;         for (int lvl = 0; lvl < 6; ++lvl) {
;             const int Wsrc = (lvl & 1) ? C_WB : C_WA, Wdst = (lvl & 1) ? C_WA : C_WB, Ms = (lvl & 1) ? C_MB : C_MA, Mts = (lvl & 1) ? C_MTB : C_MTA, Md = (lvl & 1) ? C_MA : C_MB, Mtd = (lvl & 1) ? C_MTA : C_MTB;
;             const Fr yW = LD(Wsrc, w); Fr yMt; if (lvl < 5) yMt = LD(Mts, nt);
;             Fr xM[4], xS[2];
; #pragma unroll
;             for (int i = 0; i < 4; ++i) xM[i] = LD(Ms, i);
;             if (lvl < 5) { xS[0] = LD(Ms, mt0); xS[1] = LD(Ms, mt0 + 1); }
;             const int nj = w * 16 + lr;
;             f32x4 old[4], aw[4], as[2];
; #pragma unroll
;             for (int i = 0; i < 4; ++i) old[i] = unpack4(*(const LAS v2u*)(L + Wsrc + nj * CP + (i * 16 + 4 * kq) * 2));
; #pragma unroll
;             for (int i = 0; i < 4; ++i) aw[i] = MM(xM[i], yW);
;             if (lvl < 5) {
; #pragma unroll
;                 for (int i = 0; i < 2; ++i) as[i] = MM(xS[i], yMt); }
; #pragma unroll
;             for (int i = 0; i < 4; ++i) *(LAS v2u*)(L + Wdst + nj * CP + (i * 16 + 4 * kq) * 2) = pack4(old[i] + aw[i]);
;             if (lvl < 5) {
; #pragma unroll
;                 for (int i = 0; i < 2; ++i) { const int m0 = (mt0 + i) * 16 + 4 * kq;
; #pragma unroll
;                     for (int e = 0; e < 4; ++e) *(LAS unsigned short*)(L + Md + (m0 + e) * CP + n * 2) = (unsigned short)f2bf(as[i][e]);
;                     if (lvl < 4) *(LAS v2u*)(L + Mtd + n * CP + m0 * 2) = pack4(as[i]); } }
;             if (lvl == 4) *(LAS v4u*)(L + C_KHT + lane * CP + 16 * w) = (v4u){kht[0], kht[1], kht[2], kht[3]};
;             if (lvl == 2) { if (hx) tr8_finish(tX, mX, tscr, lane);
;                             if (hy) { mX = moe_item(cit + 8, I.w_gu, I.w_down, F.ws); tr8_load(mX, tX, lane); } }
;             CBAR();
.LBB0_1092:
	ds_read_b128 v[100:103], v160
	v_add_u32_e32 v104, v129, v122
	ds_read_b128 v[106:109], v104 offset:36864
	ds_read_b128 v[110:113], v160 offset:64
	ds_read_b128 v[176:179], v104 offset:36928
	ds_read_b128 v[180:183], v160 offset:2304
	ds_read_b128 v[184:187], v160 offset:2368
	ds_read_b128 v[188:191], v160 offset:4608
	s_waitcnt lgkmcnt(2)
	v_mfma_f32_16x16x32_bf16 v[180:183], v[180:183], v[106:109], 0
	ds_read_b128 v[192:195], v144
	ds_read_b128 v[196:199], v145
	ds_read_b128 v[200:203], v160 offset:4672
	v_add_u32_e32 v68, v129, v130
	v_add_u32_e32 v105, 0xd800, v68
	v_mfma_f32_16x16x32_bf16 v[100:103], v[100:103], v[106:109], 0
	s_lshl_b32 s92, s14, 6
	s_and_b64 vcc, exec, s[64:65]
	s_waitcnt lgkmcnt(4)
	v_mfma_f32_16x16x32_bf16 v[180:183], v[184:187], v[176:179], v[180:183]
	ds_read_b128 v[184:187], v160 offset:6912
	ds_read_b128 v[204:207], v160 offset:6976
	v_mfma_f32_16x16x32_bf16 v[110:113], v[110:113], v[176:179], v[100:103]
	s_nop 2
	v_add_u32_e32 v103, 0x9000, v68
	s_waitcnt lgkmcnt(5)
	v_mfma_f32_16x16x32_bf16 v[188:191], v[188:191], v[106:109], 0
	ds_read2_b64 v[208:211], v103 offset1:4
	ds_read_b128 v[212:215], v161
	v_lshl_add_u64 v[244:245], v[244:245], 0, v[246:247]
	global_load_dwordx4 v[50:53], v[244:245], off
	ds_read_b128 v[216:219], v161 offset:64
	v_add_u32_e32 v102, v147, v143
	s_waitcnt lgkmcnt(2)
	v_lshlrev_b32_e32 v100, 16, v208
	v_mfma_f32_16x16x32_bf16 v[106:109], v[184:187], v[106:109], 0
	v_and_b32_e32 v101, 0xffff0000, v208
	v_lshlrev_b32_e32 v114, 16, v209
	v_and_b32_e32 v115, 0xffff0000, v209
	v_mfma_f32_16x16x32_bf16 v[188:191], v[200:203], v[176:179], v[188:191]
	ds_read_b128 v[200:203], v162
	ds_read_b128 v[220:223], v162 offset:64
	v_lshlrev_b32_e32 v208, 16, v210
	v_and_b32_e32 v209, 0xffff0000, v210
	v_mfma_f32_16x16x32_bf16 v[106:109], v[204:207], v[176:179], v[106:109]
	ds_read2_b64 v[176:179], v103 offset0:8 offset1:12
	v_lshlrev_b32_e32 v204, 16, v211
	v_and_b32_e32 v205, 0xffff0000, v211
	s_waitcnt lgkmcnt(4)
	v_mfma_f32_16x16x32_bf16 v[184:187], v[212:215], v[192:195], 0
	v_add_f32_e64 v112, v112, v114
	v_add_f32_e64 v113, v113, v115
	v_pk_add_f32 v[100:101], v[110:111], v[100:101]
	v_pk_add_f32 v[110:111], v[182:183], v[204:205]
	s_waitcnt lgkmcnt(3)
	v_mfma_f32_16x16x32_bf16 v[184:187], v[216:219], v[196:199], v[184:187]
	v_cvt_pk_bf16_f32 v100, v100, v101
	v_cvt_pk_bf16_f32 v101, v112, v113
	v_pk_add_f32 v[112:113], v[180:181], v[208:209]
	s_waitcnt lgkmcnt(0)
	v_lshlrev_b32_e32 v206, 16, v176
	v_and_b32_e32 v207, 0xffff0000, v176
	v_lshlrev_b32_e32 v210, 16, v177
	v_and_b32_e32 v211, 0xffff0000, v177
	v_cvt_pk_bf16_f32 v112, v112, v113
	v_cvt_pk_bf16_f32 v113, v110, v111
	v_lshlrev_b32_e32 v212, 16, v178
	v_mfma_f32_16x16x32_bf16 v[192:195], v[200:203], v[192:195], 0
	v_and_b32_e32 v213, 0xffff0000, v178
	v_lshlrev_b32_e32 v200, 16, v179
	v_and_b32_e32 v201, 0xffff0000, v179
	ds_write2_b64 v105, v[100:101], v[112:113] offset1:4
	v_pk_add_f32 v[100:101], v[190:191], v[210:211]
	v_pk_add_f32 v[110:111], v[188:189], v[206:207]
	v_pk_add_f32 v[106:107], v[106:107], v[212:213]
	v_cvt_pk_bf16_f32 v110, v110, v111
	v_cvt_pk_bf16_f32 v111, v100, v101
	v_pk_add_f32 v[100:101], v[108:109], v[200:201]
	v_cvt_pk_bf16_f32 v106, v106, v107
	v_cvt_pk_bf16_f32 v107, v100, v101
	v_bfe_u32 v68, v184, 16, 1
	ds_write2_b64 v105, v[110:111], v[106:107] offset0:8 offset1:12
	v_add3_u32 v68, v184, v68, s3
	v_add_u32_e32 v106, v146, v140
	ds_write_b16_d16_hi v106, v68
	v_bfe_u32 v68, v185, 16, 1
	v_add3_u32 v68, v185, v68, s3
	ds_write_b16_d16_hi v106, v68 offset:144
	v_lshl_add_u64 v[244:245], v[244:245], 0, v[246:247]
	global_load_dwordx4 v[54:57], v[244:245], off
	v_bfe_u32 v68, v186, 16, 1
	v_mfma_f32_16x16x32_bf16 v[176:179], v[220:223], v[196:199], v[192:195]
	v_add3_u32 v68, v186, v68, s3
	ds_write_b16_d16_hi v106, v68 offset:288
	v_bfe_u32 v68, v187, 16, 1
	v_add3_u32 v68, v187, v68, s3
	ds_write_b16_d16_hi v106, v68 offset:432
	v_cvt_pk_bf16_f32 v100, v184, v185
	v_cvt_pk_bf16_f32 v101, v186, v187
	v_add_u32_e32 v68, v147, v141
	ds_write_b64 v68, v[100:101]
	v_bfe_u32 v100, v176, 16, 1
	v_add3_u32 v100, v176, v100, s3
	v_add_u32_e32 v107, v146, v142
	ds_write_b16_d16_hi v107, v100
	v_bfe_u32 v100, v177, 16, 1
	v_add3_u32 v100, v177, v100, s3
	ds_write_b16_d16_hi v107, v100 offset:144
	v_bfe_u32 v100, v178, 16, 1
	v_add3_u32 v100, v178, v100, s3
	ds_write_b16_d16_hi v107, v100 offset:288
	v_bfe_u32 v100, v179, 16, 1
	v_add3_u32 v100, v179, v100, s3
	ds_write_b16_d16_hi v107, v100 offset:432
	v_cvt_pk_bf16_f32 v100, v176, v177
	v_cvt_pk_bf16_f32 v101, v178, v179
	ds_write_b64 v102, v[100:101]
	s_waitcnt lgkmcnt(0)
	s_barrier
; #define LAS __attribute__((address_space(3)))
; __device__ __forceinline__ unsigned f2bf(float f) { unsigned u = __builtin_bit_cast(unsigned, f); return (u + 0x7fffu + ((u >> 16) & 1u)) >> 16; }
; #define CBAR() do { asm volatile("s_waitcnt lgkmcnt(0)" ::: "memory"); __builtin_amdgcn_s_barrier(); asm volatile("" ::: "memory"); } while (0)
; __device__ __forceinline__ v2u pack4(const f32x4& v) { return (v2u){pg8::cvt_pk_bf16(v[0], v[1]), pg8::cvt_pk_bf16(v[2], v[3])}; }
; __device__ __forceinline__ void p4a_chunk(Frame& F0, const In& I) {
;     ...
;         for (int lvl = 0; lvl < 6; ++lvl) {
;             const int Wsrc = (lvl & 1) ? C_WB : C_WA, Wdst = (lvl & 1) ? C_WA : C_WB, Ms = (lvl & 1) ? C_MB : C_MA, Mts = (lvl & 1) ? C_MTB : C_MTA, Md = (lvl & 1) ? C_MA : C_MB, Mtd = (lvl & 1) ? C_MTA : C_MTB;
;             const Fr yW = LD(Wsrc, w); Fr yMt; if (lvl < 5) yMt = LD(Mts, nt);
;             Fr xM[4], xS[2];
; #pragma unroll
;             for (int i = 0; i < 4; ++i) xM[i] = LD(Ms, i);
;             if (lvl < 5) { xS[0] = LD(Ms, mt0); xS[1] = LD(Ms, mt0 + 1); }
;             const int nj = w * 16 + lr;
;             f32x4 old[4], aw[4], as[2];
; #pragma unroll
;             for (int i = 0; i < 4; ++i) old[i] = unpack4(*(const LAS v2u*)(L + Wsrc + nj * CP + (i * 16 + 4 * kq) * 2));
; #pragma unroll
;             for (int i = 0; i < 4; ++i) aw[i] = MM(xM[i], yW);
;             if (lvl < 5) {
; #pragma unroll
;                 for (int i = 0; i < 2; ++i) as[i] = MM(xS[i], yMt); }
; #pragma unroll
;             for (int i = 0; i < 4; ++i) *(LAS v2u*)(L + Wdst + nj * CP + (i * 16 + 4 * kq) * 2) = pack4(old[i] + aw[i]);
;             if (lvl < 5) {
; #pragma unroll
;                 for (int i = 0; i < 2; ++i) { const int m0 = (mt0 + i) * 16 + 4 * kq;
; #pragma unroll
;                     for (int e = 0; e < 4; ++e) *(LAS unsigned short*)(L + Md + (m0 + e) * CP + n * 2) = (unsigned short)f2bf(as[i][e]);
;                     if (lvl < 4) *(LAS v2u*)(L + Mtd + n * CP + m0 * 2) = pack4(as[i]); } }
;             if (lvl == 4) *(LAS v4u*)(L + C_KHT + lane * CP + 16 * w) = (v4u){kht[0], kht[1], kht[2], kht[3]};
;             if (lvl == 2) { if (hx) tr8_finish(tX, mX, tscr, lane);
;                             if (hy) { mX = moe_item(cit + 8, I.w_gu, I.w_down, F.ws); tr8_load(mX, tX, lane); } }
;             CBAR();
	ds_read_b128 v[108:111], v163
	ds_read_b128 v[112:115], v104 offset:55296
	ds_read_b128 v[176:179], v163 offset:64
	ds_read_b128 v[180:183], v104 offset:55360
	s_waitcnt lgkmcnt(2)
	v_mfma_f32_16x16x32_bf16 v[108:111], v[108:111], v[112:115], 0
	ds_read_b128 v[184:187], v163 offset:2304
	s_waitcnt lgkmcnt(1)
	v_mfma_f32_16x16x32_bf16 v[108:111], v[176:179], v[180:183], v[108:111]
	ds_read_b128 v[176:179], v163 offset:2368
	ds_read_b128 v[188:191], v163 offset:4608
	ds_read_b128 v[192:195], v163 offset:4672
	s_waitcnt lgkmcnt(3)
	v_mfma_f32_16x16x32_bf16 v[184:187], v[184:187], v[112:115], 0
	s_waitcnt lgkmcnt(2)
	v_mfma_f32_16x16x32_bf16 v[176:179], v[176:179], v[180:183], v[184:187]
	s_nop 5
	ds_read_b128 v[184:187], v148
	ds_read_b128 v[196:199], v149
	ds_read_b128 v[200:203], v163 offset:6912
	ds_read_b128 v[204:207], v163 offset:6976
	ds_read2_b64 v[208:211], v105 offset1:4
	ds_read_b128 v[212:215], v164
	ds_read_b128 v[216:219], v164 offset:64
	s_waitcnt lgkmcnt(2)
	v_lshlrev_b32_e32 v100, 16, v208
	v_mfma_f32_16x16x32_bf16 v[188:191], v[188:191], v[112:115], 0
	v_and_b32_e32 v101, 0xffff0000, v208
	v_lshl_add_u64 v[244:245], v[244:245], 0, v[246:247]
	global_load_dwordx4 v[58:61], v[244:245], off
	v_lshlrev_b32_e32 v208, 16, v209
	v_and_b32_e32 v209, 0xffff0000, v209
	v_mfma_f32_16x16x32_bf16 v[112:115], v[200:203], v[112:115], 0
	v_lshlrev_b32_e32 v224, 16, v210
	v_and_b32_e32 v225, 0xffff0000, v210
	v_pk_add_f32 v[110:111], v[110:111], v[208:209]
	v_mfma_f32_16x16x32_bf16 v[188:191], v[192:195], v[180:183], v[188:191]
	ds_read_b128 v[192:195], v165
	ds_read_b128 v[220:223], v165 offset:64
	v_pk_add_f32 v[100:101], v[108:109], v[100:101]
	v_mfma_f32_16x16x32_bf16 v[112:115], v[204:207], v[180:183], v[112:115]
	ds_read2_b64 v[180:183], v105 offset0:8 offset1:12
	v_lshlrev_b32_e32 v204, 16, v211
	v_and_b32_e32 v205, 0xffff0000, v211
	s_waitcnt lgkmcnt(4)
	v_mfma_f32_16x16x32_bf16 v[200:203], v[212:215], v[184:187], 0
	v_cvt_pk_bf16_f32 v100, v100, v101
	v_cvt_pk_bf16_f32 v101, v110, v111
	v_pk_add_f32 v[108:109], v[178:179], v[204:205]
	s_waitcnt lgkmcnt(3)
	v_mfma_f32_16x16x32_bf16 v[200:203], v[216:219], v[196:199], v[200:203]
	v_add_f32_e64 v110, v176, v224
	v_add_f32_e64 v111, v177, v225
	s_waitcnt lgkmcnt(0)
	v_lshlrev_b32_e32 v206, 16, v180
	v_and_b32_e32 v207, 0xffff0000, v180
	v_lshlrev_b32_e32 v210, 16, v181
	v_and_b32_e32 v211, 0xffff0000, v181
	v_cvt_pk_bf16_f32 v110, v110, v111
	v_cvt_pk_bf16_f32 v111, v108, v109
	v_lshlrev_b32_e32 v212, 16, v182
	v_mfma_f32_16x16x32_bf16 v[184:187], v[192:195], v[184:187], 0
	v_and_b32_e32 v213, 0xffff0000, v182
	v_lshlrev_b32_e32 v192, 16, v183
	v_and_b32_e32 v193, 0xffff0000, v183
	ds_write2_b64 v103, v[100:101], v[110:111] offset1:4
	v_pk_add_f32 v[100:101], v[190:191], v[210:211]
	v_pk_add_f32 v[108:109], v[188:189], v[206:207]
	v_pk_add_f32 v[110:111], v[112:113], v[212:213]
	v_cvt_pk_bf16_f32 v108, v108, v109
	v_cvt_pk_bf16_f32 v109, v100, v101
	v_pk_add_f32 v[100:101], v[114:115], v[192:193]
	v_cvt_pk_bf16_f32 v110, v110, v111
	v_cvt_pk_bf16_f32 v111, v100, v101
	v_bfe_u32 v100, v200, 16, 1
	ds_write2_b64 v103, v[108:109], v[110:111] offset0:8 offset1:12
	v_add3_u32 v100, v200, v100, s3
	v_add_u32_e32 v108, v150, v140
	ds_write_b16_d16_hi v108, v100
	v_bfe_u32 v100, v201, 16, 1
	v_add3_u32 v100, v201, v100, s3
	ds_write_b16_d16_hi v108, v100 offset:144
	v_bfe_u32 v100, v202, 16, 1
	v_mfma_f32_16x16x32_bf16 v[180:183], v[220:223], v[196:199], v[184:187]
	v_add3_u32 v100, v202, v100, s3
	v_lshl_add_u64 v[244:245], v[244:245], 0, v[246:247]
	global_load_dwordx4 v[62:65], v[244:245], off
	ds_write_b16_d16_hi v108, v100 offset:288
	v_bfe_u32 v100, v203, 16, 1
	v_add3_u32 v100, v203, v100, s3
	ds_write_b16_d16_hi v108, v100 offset:432
	v_cvt_pk_bf16_f32 v100, v200, v201
	v_cvt_pk_bf16_f32 v101, v202, v203
	v_add_u32_e32 v110, v151, v141
	ds_write_b64 v110, v[100:101]
	v_bfe_u32 v100, v180, 16, 1
	v_add3_u32 v100, v180, v100, s3
	v_add_u32_e32 v109, v150, v142
	ds_write_b16_d16_hi v109, v100
	v_bfe_u32 v100, v181, 16, 1
	v_add3_u32 v100, v181, v100, s3
	ds_write_b16_d16_hi v109, v100 offset:144
	v_bfe_u32 v100, v182, 16, 1
	v_add3_u32 v100, v182, v100, s3
	ds_write_b16_d16_hi v109, v100 offset:288
	v_bfe_u32 v100, v183, 16, 1
	v_add3_u32 v100, v183, v100, s3
	ds_write_b16_d16_hi v109, v100 offset:432
	v_cvt_pk_bf16_f32 v100, v180, v181
	v_cvt_pk_bf16_f32 v101, v182, v183
	v_add_u32_e32 v111, v151, v143
	ds_write_b64 v111, v[100:101]
	s_waitcnt lgkmcnt(0)
	s_barrier
; #define LAS __attribute__((address_space(3)))
; __device__ __forceinline__ unsigned f2bf(float f) { unsigned u = __builtin_bit_cast(unsigned, f); return (u + 0x7fffu + ((u >> 16) & 1u)) >> 16; }
; __device__ __forceinline__ v2u pack4(const f32x4& v) { return (v2u){pg8::cvt_pk_bf16(v[0], v[1]), pg8::cvt_pk_bf16(v[2], v[3])}; }
; __device__ __forceinline__ f32x4 unpack4(const v2u w) { return (f32x4){bflo(w.x), bfhi(w.x), bflo(w.y), bfhi(w.y)}; }
; __device__ __forceinline__ void p4a_chunk(Frame& F0, const In& I) {
;     ...
;         for (int lvl = 0; lvl < 6; ++lvl) {
;             const int Wsrc = (lvl & 1) ? C_WB : C_WA, Wdst = (lvl & 1) ? C_WA : C_WB, Ms = (lvl & 1) ? C_MB : C_MA, Mts = (lvl & 1) ? C_MTB : C_MTA, Md = (lvl & 1) ? C_MA : C_MB, Mtd = (lvl & 1) ? C_MTA : C_MTB;
;             const Fr yW = LD(Wsrc, w); Fr yMt; if (lvl < 5) yMt = LD(Mts, nt);
;             Fr xM[4], xS[2];
; #pragma unroll
;             for (int i = 0; i < 4; ++i) xM[i] = LD(Ms, i);
;             if (lvl < 5) { xS[0] = LD(Ms, mt0); xS[1] = LD(Ms, mt0 + 1); }
;             const int nj = w * 16 + lr;
;             f32x4 old[4], aw[4], as[2];
; #pragma unroll
;             for (int i = 0; i < 4; ++i) old[i] = unpack4(*(const LAS v2u*)(L + Wsrc + nj * CP + (i * 16 + 4 * kq) * 2));
; #pragma unroll
;             for (int i = 0; i < 4; ++i) aw[i] = MM(xM[i], yW);
;             if (lvl < 5) {
; #pragma unroll
;                 for (int i = 0; i < 2; ++i) as[i] = MM(xS[i], yMt); }
; #pragma unroll
;             for (int i = 0; i < 4; ++i) *(LAS v2u*)(L + Wdst + nj * CP + (i * 16 + 4 * kq) * 2) = pack4(old[i] + aw[i]);
;             if (lvl < 5) {
; #pragma unroll
;                 for (int i = 0; i < 2; ++i) { const int m0 = (mt0 + i) * 16 + 4 * kq;
; #pragma unroll
;                     for (int e = 0; e < 4; ++e) *(LAS unsigned short*)(L + Md + (m0 + e) * CP + n * 2) = (unsigned short)f2bf(as[i][e]);
;                     if (lvl < 4) *(LAS v2u*)(L + Mtd + n * CP + m0 * 2) = pack4(as[i]); } }
;             if (lvl == 4) *(LAS v4u*)(L + C_KHT + lane * CP + 16 * w) = (v4u){kht[0], kht[1], kht[2], kht[3]};
;             if (lvl == 2) { if (hx) tr8_finish(tX, mX, tscr, lane);
	ds_read_b128 v[112:115], v160
	ds_read_b128 v[176:179], v104 offset:36864
	ds_read_b128 v[180:183], v160 offset:64
	ds_read_b128 v[184:187], v104 offset:36928
	s_waitcnt lgkmcnt(2)
	v_mfma_f32_16x16x32_bf16 v[112:115], v[112:115], v[176:179], 0
	ds_read_b128 v[188:191], v160 offset:2304
	ds_read_b128 v[192:195], v160 offset:4608
	ds_read_b128 v[196:199], v160 offset:4672
	s_waitcnt lgkmcnt(3)
	v_mfma_f32_16x16x32_bf16 v[112:115], v[180:183], v[184:187], v[112:115]
	ds_read_b128 v[180:183], v160 offset:2368
	s_waitcnt lgkmcnt(3)
	v_mfma_f32_16x16x32_bf16 v[188:191], v[188:191], v[176:179], 0
	s_waitcnt lgkmcnt(0)
	v_mfma_f32_16x16x32_bf16 v[180:183], v[180:183], v[184:187], v[188:191]
	s_nop 5
	ds_read_b128 v[188:191], v144
	ds_read_b128 v[200:203], v145
	ds_read_b128 v[204:207], v160 offset:6912
	ds_read_b128 v[208:211], v160 offset:6976
	ds_read2_b64 v[212:215], v103 offset1:4
	ds_read_b128 v[216:219], v161
	ds_read_b128 v[220:223], v161 offset:64
	s_waitcnt lgkmcnt(2)
	v_lshlrev_b32_e32 v100, 16, v212
	v_mfma_f32_16x16x32_bf16 v[192:195], v[192:195], v[176:179], 0
	v_and_b32_e32 v101, 0xffff0000, v212
	v_lshlrev_b32_e32 v212, 16, v213
	v_and_b32_e32 v213, 0xffff0000, v213
	v_mfma_f32_16x16x32_bf16 v[176:179], v[204:207], v[176:179], 0
	v_lshlrev_b32_e32 v228, 16, v214
	v_and_b32_e32 v229, 0xffff0000, v214
	v_pk_add_f32 v[114:115], v[114:115], v[212:213]
	v_mfma_f32_16x16x32_bf16 v[192:195], v[196:199], v[184:187], v[192:195]
	ds_read_b128 v[196:199], v162
	ds_read_b128 v[224:227], v162 offset:64
	v_pk_add_f32 v[100:101], v[112:113], v[100:101]
	v_mfma_f32_16x16x32_bf16 v[176:179], v[208:211], v[184:187], v[176:179]
	ds_read2_b64 v[184:187], v103 offset0:8 offset1:12
	v_lshlrev_b32_e32 v208, 16, v215
	v_and_b32_e32 v209, 0xffff0000, v215
	s_waitcnt lgkmcnt(4)
	v_mfma_f32_16x16x32_bf16 v[204:207], v[216:219], v[188:191], 0
	v_cvt_pk_bf16_f32 v100, v100, v101
	v_cvt_pk_bf16_f32 v101, v114, v115
	v_pk_add_f32 v[112:113], v[182:183], v[208:209]
	s_waitcnt lgkmcnt(3)
	v_mfma_f32_16x16x32_bf16 v[204:207], v[220:223], v[200:203], v[204:207]
	v_add_f32_e64 v114, v180, v228
	v_add_f32_e64 v115, v181, v229
	s_waitcnt lgkmcnt(0)
	v_lshlrev_b32_e32 v210, 16, v184
	v_and_b32_e32 v211, 0xffff0000, v184
	v_lshlrev_b32_e32 v214, 16, v185
	v_and_b32_e32 v215, 0xffff0000, v185
	v_cvt_pk_bf16_f32 v114, v114, v115
	v_cvt_pk_bf16_f32 v115, v112, v113
	v_lshlrev_b32_e32 v216, 16, v186
	v_mfma_f32_16x16x32_bf16 v[188:191], v[196:199], v[188:191], 0
	v_and_b32_e32 v217, 0xffff0000, v186
	v_lshlrev_b32_e32 v196, 16, v187
	v_and_b32_e32 v197, 0xffff0000, v187
	ds_write2_b64 v105, v[100:101], v[114:115] offset1:4
	v_pk_add_f32 v[100:101], v[194:195], v[214:215]
	v_pk_add_f32 v[112:113], v[192:193], v[210:211]
	v_pk_add_f32 v[114:115], v[176:177], v[216:217]
	v_cvt_pk_bf16_f32 v112, v112, v113
	v_cvt_pk_bf16_f32 v113, v100, v101
	v_pk_add_f32 v[100:101], v[178:179], v[196:197]
	v_cvt_pk_bf16_f32 v114, v114, v115
	v_cvt_pk_bf16_f32 v115, v100, v101
	v_bfe_u32 v100, v204, 16, 1
	v_add3_u32 v100, v204, v100, s3
	ds_write2_b64 v105, v[112:113], v[114:115] offset0:8 offset1:12
	ds_write_b16_d16_hi v106, v100
	v_bfe_u32 v100, v205, 16, 1
	v_add3_u32 v100, v205, v100, s3
	ds_write_b16_d16_hi v106, v100 offset:144
	v_bfe_u32 v100, v206, 16, 1
	v_mfma_f32_16x16x32_bf16 v[184:187], v[224:227], v[200:203], v[188:191]
	v_add3_u32 v100, v206, v100, s3
	ds_write_b16_d16_hi v106, v100 offset:288
	v_bfe_u32 v100, v207, 16, 1
	v_add3_u32 v100, v207, v100, s3
	ds_write_b16_d16_hi v106, v100 offset:432
	v_cvt_pk_bf16_f32 v100, v204, v205
	v_cvt_pk_bf16_f32 v101, v206, v207
	ds_write_b64 v68, v[100:101]
	v_bfe_u32 v68, v184, 16, 1
	v_add3_u32 v68, v184, v68, s3
	ds_write_b16_d16_hi v107, v68
	v_bfe_u32 v68, v185, 16, 1
	v_add3_u32 v68, v185, v68, s3
	ds_write_b16_d16_hi v107, v68 offset:144
	v_bfe_u32 v68, v186, 16, 1
	v_add3_u32 v68, v186, v68, s3
	ds_write_b16_d16_hi v107, v68 offset:288
	v_bfe_u32 v68, v187, 16, 1
	v_add3_u32 v68, v187, v68, s3
	v_cvt_pk_bf16_f32 v100, v184, v185
	v_cvt_pk_bf16_f32 v101, v186, v187
	ds_write_b16_d16_hi v107, v68 offset:432
	ds_write_b64 v102, v[100:101]
	v_add_u32_e32 v102, 0x400, v167
	v_add_u32_e32 v101, 0x800, v167
	v_add_u32_e32 v100, 0xc00, v167
	s_cbranch_vccnz .LBB0_1094
; #define GAS __attribute__((address_space(1)))
; #define LAS __attribute__((address_space(3)))
; #define LDS_WAIT() asm volatile("s_waitcnt lgkmcnt(0)" ::: "memory")
; __device__ __forceinline__ void tr8_finish(const f32x4 (&v)[16], const MoeItem& m, LAS float* scr_, int lane) {
;     LAS unsigned char* scr = (LAS unsigned char*)scr_;
;     const int kr = lane >> 4, cq = lane & 15;
; #pragma unroll
;     for (int j = 0; j < 4; ++j) { unsigned w[4];
; #pragma unroll
;         for (int q = 0; q < 4; ++q) { s16x2 t = {0, 0};
;             t = __builtin_amdgcn_cvt_scalef32_pk_fp8_f32(t, v[4 * q][j], v[4 * q + 1][j], F8_CVT_SCALE, false);
;             t = __builtin_amdgcn_cvt_scalef32_pk_fp8_f32(t, v[4 * q + 2][j], v[4 * q + 3][j], F8_CVT_SCALE, true);
;             w[q] = __builtin_bit_cast(unsigned, t); }
;         *(LAS v4u*)(scr + (4 * cq + j) * 80 + kr * 16) = (v4u){w[0], w[1], w[2], w[3]}; }
;     LDS_WAIT(); asm volatile("" ::: "memory");
;     const int qd = lane & 3;
; #pragma unroll
;     for (int ps = 0; ps < 4; ++ps) { const int n = (lane >> 2) + 16 * ps; const LAS unsigned char* s = scr + n * 80 + qd * 4;
;         const unsigned d0 = *(const LAS unsigned*)(s), d1 = *(const LAS unsigned*)(s + 16), d2 = *(const LAS unsigned*)(s + 32), d3 = *(const LAS unsigned*)(s + 48);
;         const unsigned t0 = __builtin_amdgcn_perm(d1, d0, 0x05010400u), t1 = __builtin_amdgcn_perm(d1, d0, 0x07030602u), t2 = __builtin_amdgcn_perm(d3, d2, 0x05010400u), t3 = __builtin_amdgcn_perm(d3, d2, 0x07030602u);
;         const v4u o = (v4u){__builtin_amdgcn_perm(t2, t0, 0x05040100u), __builtin_amdgcn_perm(t2, t0, 0x07060302u), __builtin_amdgcn_perm(t3, t1, 0x05040100u), __builtin_amdgcn_perm(t3, t1, 0x07060302u)};
;         *(GAS v4u*)(m.WT + (size_t)(m.drow + n) * m.ldt + m.k0 + 16 * qd) = o; }
;     LDS_WAIT(); asm volatile("" ::: "memory");
	v_mov_b32_e32 v112, v69
	v_mov_b32_e32 v113, v69
	v_mov_b32_e32 v114, v69
	v_mov_b32_e32 v115, v69
	s_waitcnt vmcnt(10)
	v_cvt_scalef32_pk_fp8_f32 v112, v2, v6, s5
	v_cvt_scalef32_pk_fp8_f32 v113, v18, v22, s5
	s_waitcnt vmcnt(6)
	v_cvt_scalef32_pk_fp8_f32 v114, v34, v38, s5
	s_waitcnt vmcnt(2)
	v_cvt_scalef32_pk_fp8_f32 v115, v50, v54, s5
	v_cvt_scalef32_pk_fp8_f32 v112, v10, v14, s5 op_sel:[0,0,0,1]
	v_cvt_scalef32_pk_fp8_f32 v113, v26, v30, s5 op_sel:[0,0,0,1]
	v_cvt_scalef32_pk_fp8_f32 v114, v42, v46, s5 op_sel:[0,0,0,1]
	s_waitcnt vmcnt(0)
	v_cvt_scalef32_pk_fp8_f32 v115, v58, v62, s5 op_sel:[0,0,0,1]
	ds_write_b128 v166, v[112:115]
	v_mov_b32_e32 v112, v69
	v_mov_b32_e32 v113, v69
	v_mov_b32_e32 v114, v69
	v_mov_b32_e32 v115, v69
	v_cvt_scalef32_pk_fp8_f32 v112, v3, v7, s5
	v_cvt_scalef32_pk_fp8_f32 v113, v19, v23, s5
	v_cvt_scalef32_pk_fp8_f32 v114, v35, v39, s5
	v_cvt_scalef32_pk_fp8_f32 v115, v51, v55, s5
	v_cvt_scalef32_pk_fp8_f32 v112, v11, v15, s5 op_sel:[0,0,0,1]
	v_cvt_scalef32_pk_fp8_f32 v113, v27, v31, s5 op_sel:[0,0,0,1]
	v_cvt_scalef32_pk_fp8_f32 v114, v43, v47, s5 op_sel:[0,0,0,1]
	v_cvt_scalef32_pk_fp8_f32 v115, v59, v63, s5 op_sel:[0,0,0,1]
	ds_write_b128 v166, v[112:115] offset:80
	v_mov_b32_e32 v112, v69
	v_mov_b32_e32 v113, v69
	v_mov_b32_e32 v114, v69
	v_mov_b32_e32 v115, v69
	v_cvt_scalef32_pk_fp8_f32 v112, v4, v8, s5
	v_cvt_scalef32_pk_fp8_f32 v113, v20, v24, s5
	v_cvt_scalef32_pk_fp8_f32 v114, v36, v40, s5
	v_cvt_scalef32_pk_fp8_f32 v115, v52, v56, s5
	v_cvt_scalef32_pk_fp8_f32 v112, v12, v16, s5 op_sel:[0,0,0,1]
	v_cvt_scalef32_pk_fp8_f32 v113, v28, v32, s5 op_sel:[0,0,0,1]
	v_cvt_scalef32_pk_fp8_f32 v114, v44, v48, s5 op_sel:[0,0,0,1]
	v_cvt_scalef32_pk_fp8_f32 v115, v60, v64, s5 op_sel:[0,0,0,1]
	ds_write_b128 v166, v[112:115] offset:160
	v_mov_b32_e32 v112, v69
	v_mov_b32_e32 v113, v69
	v_mov_b32_e32 v114, v69
	v_mov_b32_e32 v115, v69
	v_cvt_scalef32_pk_fp8_f32 v112, v5, v9, s5
	v_cvt_scalef32_pk_fp8_f32 v113, v21, v25, s5
	v_cvt_scalef32_pk_fp8_f32 v114, v37, v41, s5
	v_cvt_scalef32_pk_fp8_f32 v115, v53, v57, s5
	v_cvt_scalef32_pk_fp8_f32 v112, v13, v17, s5 op_sel:[0,0,0,1]
	v_cvt_scalef32_pk_fp8_f32 v113, v29, v33, s5 op_sel:[0,0,0,1]
	v_cvt_scalef32_pk_fp8_f32 v114, v45, v49, s5 op_sel:[0,0,0,1]
	v_cvt_scalef32_pk_fp8_f32 v115, v61, v65, s5 op_sel:[0,0,0,1]
	ds_write_b128 v166, v[112:115] offset:240
	s_waitcnt lgkmcnt(0)
	ds_read2_b32 v[112:113], v167 offset1:4
	ds_read2_b32 v[114:115], v167 offset0:8 offset1:12
	s_ashr_i32 s93, s92, 31
	s_waitcnt lgkmcnt(1)
	v_perm_b32 v68, v113, v112, s6
	v_perm_b32 v176, v113, v112, s7
	s_waitcnt lgkmcnt(0)
	v_perm_b32 v113, v115, v114, s6
	v_perm_b32 v115, v115, v114, s7
	v_perm_b32 v112, v113, v68, s8
	v_perm_b32 v113, v113, v68, s9
	v_add_u32_e32 v68, s86, v132
	v_perm_b32 v114, v115, v176, s8
	v_perm_b32 v115, v115, v176, s9
	v_lshlrev_b64 v[176:177], 11, v[68:69]
	v_lshl_add_u64 v[176:177], s[72:73], 0, v[176:177]
	v_lshl_add_u64 v[176:177], v[176:177], 0, s[92:93]
	v_lshl_add_u64 v[176:177], v[176:177], 0, v[66:67]
	global_store_dwordx4 v[176:177], v[112:115], off
	ds_read2_b32 v[112:113], v102 offset0:64 offset1:68
	ds_read2_b32 v[114:115], v102 offset0:72 offset1:76
	s_waitcnt lgkmcnt(1)
	v_perm_b32 v68, v113, v112, s6
	v_perm_b32 v176, v113, v112, s7
	s_waitcnt lgkmcnt(0)
	v_perm_b32 v113, v115, v114, s6
	v_perm_b32 v115, v115, v114, s7
	v_perm_b32 v112, v113, v68, s8
	v_perm_b32 v113, v113, v68, s9
	v_add_u32_e32 v68, s86, v133
	v_perm_b32 v114, v115, v176, s8
	v_perm_b32 v115, v115, v176, s9
	v_lshlrev_b64 v[176:177], 11, v[68:69]
	v_lshl_add_u64 v[176:177], s[72:73], 0, v[176:177]
	v_lshl_add_u64 v[176:177], v[176:177], 0, s[92:93]
	v_lshl_add_u64 v[176:177], v[176:177], 0, v[66:67]
	global_store_dwordx4 v[176:177], v[112:115], off
	ds_read2_b32 v[112:113], v101 offset0:128 offset1:132
	ds_read2_b32 v[114:115], v101 offset0:136 offset1:140
	s_waitcnt lgkmcnt(1)
	v_perm_b32 v68, v113, v112, s6
	v_perm_b32 v176, v113, v112, s7
	s_waitcnt lgkmcnt(0)
	v_perm_b32 v113, v115, v114, s6
	v_perm_b32 v115, v115, v114, s7
	v_perm_b32 v112, v113, v68, s8
	v_perm_b32 v113, v113, v68, s9
	v_add_u32_e32 v68, s86, v134
	v_perm_b32 v114, v115, v176, s8
	v_perm_b32 v115, v115, v176, s9
	v_lshlrev_b64 v[176:177], 11, v[68:69]
	v_lshl_add_u64 v[176:177], s[72:73], 0, v[176:177]
	v_lshl_add_u64 v[176:177], v[176:177], 0, s[92:93]
	v_lshl_add_u64 v[176:177], v[176:177], 0, v[66:67]
	global_store_dwordx4 v[176:177], v[112:115], off
	ds_read2_b32 v[112:113], v100 offset0:192 offset1:196
	ds_read2_b32 v[114:115], v100 offset0:200 offset1:204
	s_waitcnt lgkmcnt(1)
	v_perm_b32 v68, v113, v112, s6
	v_perm_b32 v176, v113, v112, s7
	s_waitcnt lgkmcnt(0)
	v_perm_b32 v113, v115, v114, s6
	v_perm_b32 v115, v115, v114, s7
	v_perm_b32 v112, v113, v68, s8
	v_perm_b32 v113, v113, v68, s9
	v_add_u32_e32 v68, s86, v135
	v_perm_b32 v114, v115, v176, s8
	v_perm_b32 v115, v115, v176, s9
	v_lshlrev_b64 v[176:177], 11, v[68:69]
	v_lshl_add_u64 v[176:177], s[72:73], 0, v[176:177]
	v_lshl_add_u64 v[176:177], v[176:177], 0, s[92:93]
	v_lshl_add_u64 v[176:177], v[176:177], 0, v[66:67]
	global_store_dwordx4 v[176:177], v[112:115], off
	s_waitcnt lgkmcnt(0)
; __device__ __forceinline__ void tr8_load(const MoeItem& m, f32x4 (&v)[16], int lane) {
;     const int kr = lane >> 4, cq = lane & 15;
;     const int voff = (kr * m.ldw + 4 * cq) * 4;
; #pragma unroll
;     for (int i = 0; i < 16; ++i) v[i] = __builtin_bit_cast(f32x4, __builtin_amdgcn_raw_buffer_load_b128(m.rs, voff, (int)(m.soff + (unsigned)i * m.rstep), 0));
; }
; __device__ __forceinline__ MoeItem moe_item(int r, const float* w_gu, const float* w_down, unsigned char* ws) {
;     MoeItem m;
;     if (r < MOE_J4) { const int e = r / 2048, q = r % 2048, kb = q / 64, cb = q % 64, c0 = cb * 64; const int cc = c0 & 2047;
;         m.rs = __builtin_amdgcn_make_buffer_rsrc((void*)w_gu, 0, 0xffffffff, 0x00020000); m.ldw = 2 * FF; m.k0 = kb * 64;
;         m.soff = (unsigned)(((size_t)e * D * 2 * FF + (size_t)kb * 64 * (2 * FF) + c0) * 4); m.rstep = 4u * (2 * FF) * 4u;
;         m.WT = ws + WS_WGUT + (size_t)e * 2 * FF * D; m.ldt = D; m.drow = (cc >> 7) * 256 + (c0 >= 2048 ? 128 : 0) + (cc & 127); }
;     else { r -= MOE_J4; const int e = r / 1024, q = r % 1024, kb = q / 32, cb = q % 32;
;         m.rs = __builtin_amdgcn_make_buffer_rsrc((void*)w_down, 0, 0xffffffff, 0x00020000); m.ldw = D; m.k0 = kb * 64;
;         m.soff = (unsigned)(((size_t)e * FF * D + (size_t)kb * 64 * D + cb * 64) * 4); m.rstep = 4u * D * 4u;
;         m.WT = ws + WS_WDNT + (size_t)e * D * FF; m.ldt = FF; m.drow = cb * 64; }
;     return m;
.LBB0_1094:
	v_cndmask_b32_e64 v68, 0, 1, s[70:71]
	v_cmp_ne_u32_e64 s[64:65], 1, v68
	s_andn2_b64 vcc, exec, s[70:71]
	s_cbranch_vccnz .LBB0_1096
	s_add_i32 s16, s85, 8
	s_add_i32 s14, s85, 0xffff0008
	s_lshr_b32 s86, s14, 10
	s_bfe_u32 s17, s16, 0x50005
	s_lshl_b64 s[14:15], s[86:87], 22
	s_lshl_b32 s72, s17, 17
	s_and_b32 s74, s91, 0x7c0
	s_or_b32 s72, s72, s14
	s_or_b32 s72, s72, s74
	s_add_u32 s75, s68, s14
	s_addc_u32 s73, s69, s15
	s_ashr_i32 s14, s16, 31
	s_lshr_b32 s14, s14, 21
	s_add_i32 s15, s16, s14
	s_ashr_i32 s14, s15, 11
	s_and_b32 s15, s15, 0xf800
	s_sub_i32 s15, s16, s15
	s_sext_i32_i16 s16, s15
	s_bfe_u32 s16, s16, 0x60019
	s_add_i32 s16, s15, s16
	s_sext_i32_i16 s86, s16
	s_and_b32 s16, s16, 0xffc0
	s_ashr_i32 s86, s86, 6
	s_sub_i32 s15, s15, s16
	s_sext_i32_i16 s16, s15
	s_lshl_b32 s93, s14, 23
	s_lshl_b32 vcc_lo, s86, 18
	s_lshl_b32 s92, s16, 6
	s_ashr_i32 s15, s14, 31
	s_add_i32 s93, vcc_lo, s93
	s_add_i32 s93, s93, s92
	s_lshl_b64 s[14:15], s[14:15], 23
	s_add_u32 s14, s80, s14
	v_readlane_b32 s20, v255, 13
	s_addc_u32 s15, s20, s15
	s_lshl_b32 vcc_lo, s16, 7
	s_and_b32 vcc_lo, vcc_lo, 0xf00
	s_cmp_gt_i32 s16, 31
	s_cselect_b32 s16, 0x80, 0
	s_or_b32 s16, vcc_lo, s16
	s_and_b32 s92, s92, 64
	s_or_b32 s16, s16, s92
	s_cmp_lt_i32 s85, 0xfff8
	s_cselect_b32 vcc_hi, s93, s72
	s_mov_b32 s93, 0xa0000
	v_readlane_b32 s48, v254, 37
	s_cselect_b32 s20, s93, 0x50000
	s_mov_b32 s93, 0xc0000
	v_readlane_b32 s49, v254, 38
	v_readlane_b32 s52, v254, 41
	v_readlane_b32 s53, v254, 42
	v_readlane_b32 s54, v254, 43
	s_mov_b32 s72, 0x10000
	s_mov_b32 s48, s22
	s_cselect_b32 s22, s93, 0x60000
	s_mov_b32 s93, 0xe0000
	v_readlane_b32 s50, v254, 39
	v_readlane_b32 s51, v254, 40
	v_readlane_b32 s58, v254, 47
	v_readlane_b32 s59, v254, 48
	v_readlane_b32 s62, v254, 51
	v_readlane_b32 s63, v254, 52
	s_mov_b32 s52, s68
	s_cselect_b32 s68, s72, 0x8000
	s_cselect_b32 s17, s86, s17
	s_cselect_b32 s73, s15, s73
	s_cselect_b32 s72, s14, s75
	s_cselect_b32 s86, s16, s74
	s_cselect_b32 s14, 12, 11
	s_mov_b32 s15, 0x30000
	s_mov_b32 s16, 0x50000
	s_mov_b32 s53, s69
	s_mov_b32 s69, 0x60000
	s_mov_b32 s74, 0x70000
	s_mov_b32 s75, 0x90000
	s_mov_b32 s21, 0xb0000
	s_mov_b32 s49, s23
	s_mov_b32 s23, 0xd0000
	s_mov_b32 s54, s80
	s_cselect_b32 s80, s93, 0x70000
	s_mov_b32 s93, 0xf0000
	s_cselect_b32 s92, s58, s62
	s_cselect_b32 vcc_lo, s59, s63
	s_cselect_b32 s15, s15, 0x18000
	s_cselect_b32 s16, s16, 0x28000
	s_cselect_b32 s69, s69, 0x30000
	s_cselect_b32 s74, s74, 0x38000
	s_cselect_b32 s75, s75, 0x48000
	s_cselect_b32 s21, s21, 0x58000
	s_cselect_b32 s23, s23, 0x68000
	s_mov_b64 s[50:51], s[24:25]
	s_cselect_b32 s24, s93, 0x78000
	s_lshl_b32 s25, vcc_hi, 2
	s_nop 0
	v_lshl_or_b32 v2, v116, s14, v128
	s_and_b32 s93, vcc_lo, 0xffff
	s_nop 0
	v_lshlrev_b32_e32 v62, 2, v2
	s_add_i32 s14, s25, s68
	buffer_load_dwordx4 v[2:5], v62, s[92:95], s25 offen
	buffer_load_dwordx4 v[6:9], v62, s[92:95], s14 offen
	s_add_i32 s14, s14, s68
	s_add_i32 s15, s25, s15
	s_add_i32 vcc_hi, vcc_hi, s68
	buffer_load_dwordx4 v[10:13], v62, s[92:95], s14 offen
	buffer_load_dwordx4 v[14:17], v62, s[92:95], s15 offen
	s_lshl_b32 s15, vcc_hi, 2
	s_mul_i32 s68, s68, 6
	s_add_i32 s16, s25, s16
	buffer_load_dwordx4 v[18:21], v62, s[92:95], s15 offen
	buffer_load_dwordx4 v[22:25], v62, s[92:95], s16 offen
	s_add_i32 s15, s25, s69
	s_add_i32 s14, s14, s68
	s_add_i32 s16, s25, s74
	buffer_load_dwordx4 v[26:29], v62, s[92:95], s15 offen
	buffer_load_dwordx4 v[30:33], v62, s[92:95], s16 offen
	s_add_i32 s15, s25, s75
	buffer_load_dwordx4 v[34:37], v62, s[92:95], s14 offen
	buffer_load_dwordx4 v[38:41], v62, s[92:95], s15 offen
	s_add_i32 s14, s25, s20
	s_add_i32 s15, s25, s21
	buffer_load_dwordx4 v[42:45], v62, s[92:95], s14 offen
	buffer_load_dwordx4 v[46:49], v62, s[92:95], s15 offen
	s_add_i32 s14, s25, s22
	s_add_i32 s15, s25, s23
	buffer_load_dwordx4 v[50:53], v62, s[92:95], s14 offen
	buffer_load_dwordx4 v[54:57], v62, s[92:95], s15 offen
	s_add_i32 s14, s25, s80
	s_add_i32 s25, s25, s24
	buffer_load_dwordx4 v[58:61], v62, s[92:95], s14 offen
	s_nop 0
	buffer_load_dwordx4 v[62:65], v62, s[92:95], s25 offen
	s_mov_b32 s69, s53
	s_mov_b32 s68, s52
	s_mov_b32 s22, s48
	s_mov_b32 s23, s49
	s_mov_b32 s80, s54
	s_mov_b64 s[24:25], s[50:51]
	s_lshl_b32 s92, s17, 6
	v_readlane_b32 s55, v254, 44
	v_readlane_b32 s56, v254, 45
	v_readlane_b32 s57, v254, 46
	v_readlane_b32 s60, v254, 49
	v_readlane_b32 s61, v254, 50
